# v15_g_k2
# speedup vs baseline: 1.0417x; 1.0409x over previous
.LBB3_4:
	s_ashr_i32 s20, s3, 31
	s_mov_b32 s50, 0
	s_lshr_b32 s20, s20, 26
	s_add_i32 s20, s3, s20
	s_ashr_i32 s51, s50, 31
	s_ashr_i32 s94, s20, 6
	s_lshl_b64 s[56:57], s[50:51], 1
	s_add_u32 s20, s36, s56
	s_addc_u32 s21, s37, s57
	s_add_u32 s56, s30, s56
	s_addc_u32 s57, s31, s57
	v_lshl_add_u64 v[18:19], s[56:57], 0, v[108:109]
	v_add_co_u32_e32 v2, vcc, s35, v18
	s_nop 1
	v_addc_co_u32_e32 v3, vcc, 0, v19, vcc
	v_add_co_u32_e32 v4, vcc, s41, v18
	s_barrier
	s_nop 0
	v_addc_co_u32_e32 v5, vcc, 0, v19, vcc
	global_load_dwordx4 v[22:25], v106, s[56:57]
	global_load_dwordx4 v[26:29], v[2:3], off offset:1024
	global_load_dwordx4 v[30:33], v[4:5], off offset:2048
	v_add_co_u32_e32 v2, vcc, s43, v18
	s_mul_i32 s95, s94, 0x50
	s_nop 0
	v_addc_co_u32_e32 v3, vcc, 0, v19, vcc
	v_add_co_u32_e32 v4, vcc, s45, v18
	v_add_u32_e32 v42, s95, v1
	s_nop 0
	v_addc_co_u32_e32 v5, vcc, 0, v19, vcc
	global_load_dwordx4 v[34:37], v[2:3], off offset:3072
	global_load_dwordx4 v[38:41], v[4:5], off
	v_add_co_u32_e32 v2, vcc, s47, v18
	s_mul_i32 s58, s94, 0xffe9a800
	s_nop 0
	v_addc_co_u32_e32 v3, vcc, 0, v19, vcc
	v_add_co_u32_e32 v6, vcc, s33, v18
	v_max_i32_e32 v42, 3, v42
	s_nop 0
	v_addc_co_u32_e32 v7, vcc, 0, v19, vcc
	s_add_i32 s58, s58, s29
	v_add_co_u32_e32 v10, vcc, s49, v18
	v_add_u32_e32 v42, -3, v42
	v_add_u32_e32 v44, s95, v112
	v_addc_co_u32_e32 v11, vcc, 0, v19, vcc
	v_min_u32_e32 v66, 0x400, v42
	v_add_u32_e32 v42, s58, v133
	v_max_i32_e32 v44, 3, v44
	v_add_co_u32_e32 v14, vcc, s60, v18
	v_ashrrev_i32_e32 v43, 31, v42
	v_add_u32_e32 v44, -3, v44
	v_addc_co_u32_e32 v15, vcc, 0, v19, vcc
	v_lshl_add_u64 v[42:43], v[66:67], 0, v[42:43]
	v_min_u32_e32 v66, 0x400, v44
	v_add_u32_e32 v44, s58, v132
	v_add_co_u32_e32 v18, vcc, s61, v18
	v_ashrrev_i32_e32 v45, 31, v44
	s_nop 0
	v_addc_co_u32_e32 v19, vcc, 0, v19, vcc
	v_lshl_add_u64 v[42:43], v[42:43], 4, s[20:21]
	v_lshl_add_u64 v[44:45], v[66:67], 0, v[44:45]
	global_load_dwordx4 v[2:5], v[2:3], off offset:1024
	s_nop 0
	global_load_dwordx4 v[6:9], v[6:7], off offset:2048
	s_nop 0
	global_load_dwordx4 v[10:13], v[10:11], off offset:3072
	s_nop 0
	global_load_dwordx4 v[14:17], v[14:15], off
	v_lshl_add_u64 v[44:45], v[44:45], 4, s[20:21]
	global_load_dwordx4 v[18:21], v[18:19], off offset:1024
	s_nop 0
	global_load_dwordx4 v[62:65], v[42:43], off
	global_load_dwordx4 v[58:61], v[44:45], off
	v_add_u32_e32 v42, s95, v113
	v_max_i32_e32 v42, 3, v42
	v_add_u32_e32 v42, -3, v42
	v_add_u32_e32 v44, s95, v114
	v_min_u32_e32 v66, 0x400, v42
	v_add_u32_e32 v42, s58, v131
	v_max_i32_e32 v44, 3, v44
	v_ashrrev_i32_e32 v43, 31, v42
	v_add_u32_e32 v44, -3, v44
	v_lshl_add_u64 v[42:43], v[66:67], 0, v[42:43]
	v_min_u32_e32 v66, 0x400, v44
	v_add_u32_e32 v44, s58, v130
	v_ashrrev_i32_e32 v45, 31, v44
	v_lshl_add_u64 v[42:43], v[42:43], 4, s[20:21]
	v_lshl_add_u64 v[44:45], v[66:67], 0, v[44:45]
	v_lshl_add_u64 v[44:45], v[44:45], 4, s[20:21]
	global_load_dwordx4 v[54:57], v[42:43], off
	global_load_dwordx4 v[50:53], v[44:45], off
	v_add_u32_e32 v42, s95, v115
	v_max_i32_e32 v42, 3, v42
	v_add_u32_e32 v42, -3, v42
	v_add_u32_e32 v44, s95, v116
	v_min_u32_e32 v66, 0x400, v42
	v_add_u32_e32 v42, s58, v105
	v_max_i32_e32 v44, 3, v44
	v_ashrrev_i32_e32 v43, 31, v42
	v_add_u32_e32 v44, -3, v44
	v_lshl_add_u64 v[42:43], v[66:67], 0, v[42:43]
	v_min_u32_e32 v66, 0x400, v44
	v_add_u32_e32 v44, s58, v99
	v_ashrrev_i32_e32 v45, 31, v44
	v_lshl_add_u64 v[44:45], v[66:67], 0, v[44:45]
	v_lshl_add_u64 v[42:43], v[42:43], 4, s[20:21]
	v_lshl_add_u64 v[44:45], v[44:45], 4, s[20:21]
	global_load_dwordx4 v[46:49], v[42:43], off
	s_nop 0
	global_load_dwordx4 v[42:45], v[44:45], off
	s_cmp_gt_i32 s3, 63
	s_cbranch_scc0 .LBB3_22
	s_and_saveexec_b64 s[58:59], s[8:9]
.LBB3_6:
	s_or_b64 exec, exec, s[58:59]
	s_and_saveexec_b64 s[20:21], s[10:11]

.LBB3_12:
	s_or_b64 exec, exec, s[20:21]
	v_mov_b32_e32 v107, v67
	ds_write_b128 v123, v[22:25] offset:35776
	ds_write_b128 v124, v[26:29] offset:40896
	ds_write_b128 v125, v[30:33] offset:46016
	ds_write_b128 v126, v[34:37] offset:51136
	ds_write_b128 v127, v[38:41] offset:56256
	v_lshl_add_u64 v[22:23], s[56:57], 0, v[106:107]
	v_add_co_u32_e32 v24, vcc, 0xc000, v22
	s_waitcnt lgkmcnt(0)
	s_nop 0
	v_addc_co_u32_e32 v25, vcc, 0, v23, vcc
	v_add_co_u32_e32 v28, vcc, 0xd000, v22
	s_barrier
	s_nop 0
	v_addc_co_u32_e32 v29, vcc, 0, v23, vcc
	v_add_co_u32_e32 v32, vcc, 0xf000, v22
	s_nop 1
	v_addc_co_u32_e32 v33, vcc, 0, v23, vcc
	v_add_co_u32_e32 v36, vcc, 0x10000, v22
	global_load_dwordx4 v[24:27], v[24:25], off offset:2048
	s_nop 0
	global_load_dwordx4 v[28:31], v[28:29], off offset:3072
	v_addc_co_u32_e32 v37, vcc, 0, v23, vcc
	v_add_co_u32_e32 v40, vcc, 0x11000, v22
	global_load_dwordx4 v[32:35], v[32:33], off
	s_nop 0
	global_load_dwordx4 v[36:39], v[36:37], off offset:1024
	v_addc_co_u32_e32 v41, vcc, 0, v23, vcc
	global_load_dwordx4 v[40:43], v[40:41], off offset:2048
	s_waitcnt vmcnt(5)
	ds_read_b128 v[44:47], v129 offset:35776
	ds_read_b128 v[48:51], v144
	ds_read_b128 v[52:55], v144 offset:64
	ds_read_b128 v[56:59], v129 offset:35840
	ds_read_b128 v[60:63], v129 offset:42432
	ds_read_b128 v[152:155], v129 offset:42496
	ds_read_b128 v[156:159], v129 offset:49088
	ds_read_b128 v[160:163], v129 offset:49152
	s_waitcnt lgkmcnt(6)
	v_mfma_f32_16x16x32_f16 v[44:47], v[44:47], v[48:51], 0
	ds_read_b128 v[164:167], v129 offset:55744
	ds_read_b128 v[168:171], v129 offset:55808
	s_waitcnt lgkmcnt(5)
	v_mfma_f32_16x16x32_f16 v[60:63], v[60:63], v[48:51], 0
	v_mfma_f32_16x16x32_f16 v[44:47], v[56:59], v[52:55], v[44:47]
	s_waitcnt lgkmcnt(4)
	v_mfma_f32_16x16x32_f16 v[56:59], v[152:155], v[52:55], v[60:63]
	ds_read_b128 v[152:155], v129 offset:35904
	s_waitcnt lgkmcnt(4)
	v_mfma_f32_16x16x32_f16 v[156:159], v[156:159], v[48:51], 0
	s_waitcnt lgkmcnt(2)
	v_mfma_f32_16x16x32_f16 v[48:51], v[164:167], v[48:51], 0
	v_mfma_f32_16x16x32_f16 v[60:63], v[160:163], v[52:55], v[156:159]
	s_waitcnt lgkmcnt(1)
	v_mfma_f32_16x16x32_f16 v[48:51], v[168:171], v[52:55], v[48:51]
	ds_read_b128 v[52:55], v144 offset:128
	s_nop 1
	ds_read_b128 v[156:159], v144 offset:192
	ds_read_b128 v[160:163], v129 offset:35968
	s_waitcnt lgkmcnt(2)
	v_mfma_f32_16x16x32_f16 v[44:47], v[152:155], v[52:55], v[44:47]
	ds_read_b128 v[152:155], v129 offset:42560
	ds_read_b128 v[164:167], v129 offset:42624
	s_waitcnt lgkmcnt(1)
	v_mfma_f32_16x16x32_f16 v[56:59], v[152:155], v[52:55], v[56:59]
	ds_read_b128 v[152:155], v129 offset:49216
	ds_read_b128 v[168:171], v129 offset:49280
	s_waitcnt lgkmcnt(1)
	v_mfma_f32_16x16x32_f16 v[60:63], v[152:155], v[52:55], v[60:63]
	ds_read_b128 v[152:155], v129 offset:55872
	ds_read_b128 v[172:175], v129 offset:55936
	s_waitcnt lgkmcnt(1)
	v_mfma_f32_16x16x32_f16 v[48:51], v[152:155], v[52:55], v[48:51]
	v_mfma_f32_16x16x32_f16 v[44:47], v[160:163], v[156:159], v[44:47]
	ds_read_b128 v[52:55], v144 offset:256
	ds_read_b128 v[152:155], v144 offset:320
	ds_read_b128 v[160:163], v129 offset:36032
	ds_read_b128 v[176:179], v129 offset:36096
	v_mfma_f32_16x16x32_f16 v[56:59], v[164:167], v[156:159], v[56:59]
	ds_read_b128 v[164:167], v129 offset:42688
	ds_read_b128 v[180:183], v129 offset:42752
	ds_read_b128 v[184:187], v129 offset:49344
	ds_read_b128 v[188:191], v129 offset:49408
	v_mfma_f32_16x16x32_f16 v[60:63], v[168:171], v[156:159], v[60:63]
	ds_read_b128 v[168:171], v129 offset:56000
	ds_read_b128 v[192:195], v129 offset:56064
	s_waitcnt lgkmcnt(0)
	s_barrier
	v_mfma_f32_16x16x32_f16 v[48:51], v[172:175], v[156:159], v[48:51]
	ds_write_b128 v123, v[2:5] offset:35776
	ds_write_b128 v124, v[6:9] offset:40896
	ds_write_b128 v125, v[10:13] offset:46016
	ds_write_b128 v126, v[14:17] offset:51136
	ds_write_b128 v127, v[18:21] offset:56256
	v_add_co_u32_e32 v18, vcc, s75, v22
	v_mfma_f32_16x16x32_f16 v[2:5], v[160:163], v[52:55], v[44:47]
	s_nop 0
	v_addc_co_u32_e32 v19, vcc, 0, v23, vcc
	s_waitcnt lgkmcnt(0)
	v_add_co_u32_e32 v44, vcc, s76, v22
	v_mfma_f32_16x16x32_f16 v[14:17], v[168:171], v[52:55], v[48:51]
	s_nop 0
	v_addc_co_u32_e32 v45, vcc, 0, v23, vcc
	s_barrier
	v_add_co_u32_e32 v48, vcc, s77, v22
	v_mfma_f32_16x16x32_f16 v[6:9], v[164:167], v[52:55], v[56:59]
	s_nop 0
	v_addc_co_u32_e32 v49, vcc, 0, v23, vcc
	v_mfma_f32_16x16x32_f16 v[10:13], v[184:187], v[52:55], v[60:63]
	v_add_co_u32_e32 v52, vcc, s78, v22
	global_load_dwordx4 v[18:21], v[18:19], off offset:3072
	s_nop 0
	global_load_dwordx4 v[44:47], v[44:45], off
	v_addc_co_u32_e32 v53, vcc, 0, v23, vcc
	v_add_co_u32_e32 v56, vcc, s79, v22
	global_load_dwordx4 v[48:51], v[48:49], off offset:1024
	s_nop 0
	global_load_dwordx4 v[52:55], v[52:53], off offset:2048
	v_addc_co_u32_e32 v57, vcc, 0, v23, vcc
	global_load_dwordx4 v[56:59], v[56:57], off offset:3072
	v_mfma_f32_16x16x32_f16 v[2:5], v[176:179], v[152:155], v[2:5]
	v_mfma_f32_16x16x32_f16 v[6:9], v[180:183], v[152:155], v[6:9]
	v_mfma_f32_16x16x32_f16 v[10:13], v[188:191], v[152:155], v[10:13]
	v_mfma_f32_16x16x32_f16 v[14:17], v[192:195], v[152:155], v[14:17]
	ds_read_b128 v[60:63], v129 offset:35776
	ds_read_b128 v[152:155], v144 offset:416
	ds_read_b128 v[156:159], v144 offset:480
	ds_read_b128 v[160:163], v129 offset:35840
	s_waitcnt lgkmcnt(2)
	v_mfma_f32_16x16x32_f16 v[2:5], v[60:63], v[152:155], v[2:5]
	ds_read_b128 v[60:63], v129 offset:42432
	ds_read_b128 v[164:167], v129 offset:42496
	s_waitcnt lgkmcnt(1)
	v_mfma_f32_16x16x32_f16 v[6:9], v[60:63], v[152:155], v[6:9]
	ds_read_b128 v[60:63], v129 offset:49088
	ds_read_b128 v[168:171], v129 offset:49152
	s_waitcnt lgkmcnt(1)
	v_mfma_f32_16x16x32_f16 v[10:13], v[60:63], v[152:155], v[10:13]
	ds_read_b128 v[60:63], v129 offset:55744
	ds_read_b128 v[172:175], v129 offset:55808
	s_waitcnt lgkmcnt(1)
	v_mfma_f32_16x16x32_f16 v[14:17], v[60:63], v[152:155], v[14:17]
	ds_read_b128 v[60:63], v129 offset:35904
	v_mfma_f32_16x16x32_f16 v[2:5], v[160:163], v[156:159], v[2:5]
	v_mfma_f32_16x16x32_f16 v[6:9], v[164:167], v[156:159], v[6:9]
	v_mfma_f32_16x16x32_f16 v[10:13], v[168:171], v[156:159], v[10:13]
	s_waitcnt lgkmcnt(1)
	v_mfma_f32_16x16x32_f16 v[14:17], v[172:175], v[156:159], v[14:17]
	ds_read_b128 v[152:155], v144 offset:544
	ds_read_b128 v[156:159], v144 offset:608
	ds_read_b128 v[160:163], v129 offset:35968
	s_waitcnt lgkmcnt(2)
	v_mfma_f32_16x16x32_f16 v[2:5], v[60:63], v[152:155], v[2:5]
	ds_read_b128 v[60:63], v129 offset:42560
	ds_read_b128 v[164:167], v129 offset:42624
	s_waitcnt lgkmcnt(1)
	v_mfma_f32_16x16x32_f16 v[6:9], v[60:63], v[152:155], v[6:9]
	ds_read_b128 v[60:63], v129 offset:49216
	ds_read_b128 v[168:171], v129 offset:49280
	s_waitcnt lgkmcnt(1)
	v_mfma_f32_16x16x32_f16 v[10:13], v[60:63], v[152:155], v[10:13]
	ds_read_b128 v[60:63], v129 offset:55872
	ds_read_b128 v[172:175], v129 offset:55936
	s_waitcnt lgkmcnt(1)
	v_mfma_f32_16x16x32_f16 v[14:17], v[60:63], v[152:155], v[14:17]
	v_mfma_f32_16x16x32_f16 v[2:5], v[160:163], v[156:159], v[2:5]
	ds_read_b128 v[60:63], v144 offset:672
	ds_read_b128 v[152:155], v144 offset:736
	ds_read_b128 v[160:163], v129 offset:36032
	ds_read_b128 v[176:179], v129 offset:36096
	v_mfma_f32_16x16x32_f16 v[6:9], v[164:167], v[156:159], v[6:9]
	ds_read_b128 v[164:167], v129 offset:42688
	ds_read_b128 v[180:183], v129 offset:42752
	ds_read_b128 v[184:187], v129 offset:49344
	ds_read_b128 v[188:191], v129 offset:49408
	v_mfma_f32_16x16x32_f16 v[10:13], v[168:171], v[156:159], v[10:13]
	ds_read_b128 v[168:171], v129 offset:56000
	ds_read_b128 v[192:195], v129 offset:56064
	s_waitcnt lgkmcnt(0)
	s_barrier
	s_waitcnt vmcnt(9)
	ds_write_b128 v123, v[24:27] offset:35776
	s_waitcnt vmcnt(8)
	ds_write_b128 v124, v[28:31] offset:40896
	v_add_co_u32_e32 v24, vcc, s80, v22
	s_waitcnt vmcnt(7)
	ds_write_b128 v125, v[32:35] offset:46016
	s_waitcnt vmcnt(6)
	ds_write_b128 v126, v[36:39] offset:51136
	s_waitcnt vmcnt(5)
	ds_write_b128 v127, v[40:43] offset:56256
	v_addc_co_u32_e32 v25, vcc, 0, v23, vcc
	v_add_co_u32_e32 v28, vcc, s81, v22
	s_waitcnt lgkmcnt(0)
	s_nop 0
	v_addc_co_u32_e32 v29, vcc, 0, v23, vcc
	v_add_co_u32_e32 v32, vcc, s82, v22
	s_barrier
	s_nop 0
	v_addc_co_u32_e32 v33, vcc, 0, v23, vcc
	v_add_co_u32_e32 v36, vcc, s83, v22
	s_nop 1
	v_addc_co_u32_e32 v37, vcc, 0, v23, vcc
	v_add_co_u32_e32 v40, vcc, s84, v22
	global_load_dwordx4 v[24:27], v[24:25], off
	s_nop 0
	global_load_dwordx4 v[28:31], v[28:29], off offset:1024
	s_nop 0
	global_load_dwordx4 v[32:35], v[32:33], off offset:2048
	s_nop 0
	global_load_dwordx4 v[36:39], v[36:37], off offset:3072
	v_addc_co_u32_e32 v41, vcc, 0, v23, vcc
	global_load_dwordx4 v[40:43], v[40:41], off
	v_mfma_f32_16x16x32_f16 v[14:17], v[172:175], v[156:159], v[14:17]
	v_mfma_f32_16x16x32_f16 v[2:5], v[160:163], v[60:63], v[2:5]
	v_mfma_f32_16x16x32_f16 v[6:9], v[164:167], v[60:63], v[6:9]
	v_mfma_f32_16x16x32_f16 v[10:13], v[184:187], v[60:63], v[10:13]
	v_mfma_f32_16x16x32_f16 v[14:17], v[168:171], v[60:63], v[14:17]
	v_mfma_f32_16x16x32_f16 v[2:5], v[176:179], v[152:155], v[2:5]
	v_mfma_f32_16x16x32_f16 v[6:9], v[180:183], v[152:155], v[6:9]
	v_mfma_f32_16x16x32_f16 v[10:13], v[188:191], v[152:155], v[10:13]
	v_mfma_f32_16x16x32_f16 v[14:17], v[192:195], v[152:155], v[14:17]
	ds_read_b128 v[60:63], v129 offset:35776
	ds_read_b128 v[152:155], v144 offset:832
	ds_read_b128 v[156:159], v144 offset:896
	ds_read_b128 v[160:163], v129 offset:35840
	s_waitcnt lgkmcnt(2)
	v_mfma_f32_16x16x32_f16 v[2:5], v[60:63], v[152:155], v[2:5]
	ds_read_b128 v[60:63], v129 offset:42432
	ds_read_b128 v[164:167], v129 offset:42496
	s_waitcnt lgkmcnt(1)
	v_mfma_f32_16x16x32_f16 v[6:9], v[60:63], v[152:155], v[6:9]
	ds_read_b128 v[60:63], v129 offset:49088
	ds_read_b128 v[168:171], v129 offset:49152
	s_waitcnt lgkmcnt(1)
	v_mfma_f32_16x16x32_f16 v[10:13], v[60:63], v[152:155], v[10:13]
	ds_read_b128 v[60:63], v129 offset:55744
	ds_read_b128 v[172:175], v129 offset:55808
	s_waitcnt lgkmcnt(1)
	v_mfma_f32_16x16x32_f16 v[14:17], v[60:63], v[152:155], v[14:17]
	ds_read_b128 v[60:63], v129 offset:35904
	v_mfma_f32_16x16x32_f16 v[2:5], v[160:163], v[156:159], v[2:5]
	v_mfma_f32_16x16x32_f16 v[6:9], v[164:167], v[156:159], v[6:9]
	v_mfma_f32_16x16x32_f16 v[10:13], v[168:171], v[156:159], v[10:13]
	s_waitcnt lgkmcnt(1)
	v_mfma_f32_16x16x32_f16 v[14:17], v[172:175], v[156:159], v[14:17]
	ds_read_b128 v[152:155], v144 offset:960
	ds_read_b128 v[156:159], v144 offset:1024
	ds_read_b128 v[160:163], v129 offset:35968
	s_waitcnt lgkmcnt(2)
	v_mfma_f32_16x16x32_f16 v[2:5], v[60:63], v[152:155], v[2:5]
	ds_read_b128 v[60:63], v129 offset:42560
	ds_read_b128 v[164:167], v129 offset:42624
	s_waitcnt lgkmcnt(1)
	v_mfma_f32_16x16x32_f16 v[6:9], v[60:63], v[152:155], v[6:9]
	ds_read_b128 v[60:63], v129 offset:49216
	ds_read_b128 v[168:171], v129 offset:49280
	s_waitcnt lgkmcnt(1)
	v_mfma_f32_16x16x32_f16 v[10:13], v[60:63], v[152:155], v[10:13]
	ds_read_b128 v[60:63], v129 offset:55872
	ds_read_b128 v[172:175], v129 offset:55936
	s_waitcnt lgkmcnt(1)
	v_mfma_f32_16x16x32_f16 v[14:17], v[60:63], v[152:155], v[14:17]
	v_mfma_f32_16x16x32_f16 v[2:5], v[160:163], v[156:159], v[2:5]
	ds_read_b128 v[60:63], v144 offset:1088
	ds_read_b128 v[152:155], v144 offset:1152
	ds_read_b128 v[160:163], v129 offset:36032
	ds_read_b128 v[176:179], v129 offset:36096
	v_mfma_f32_16x16x32_f16 v[6:9], v[164:167], v[156:159], v[6:9]
	ds_read_b128 v[164:167], v129 offset:42688
	ds_read_b128 v[180:183], v129 offset:42752
	ds_read_b128 v[184:187], v129 offset:49344
	ds_read_b128 v[188:191], v129 offset:49408
	v_mfma_f32_16x16x32_f16 v[10:13], v[168:171], v[156:159], v[10:13]
	ds_read_b128 v[168:171], v129 offset:56000
	ds_read_b128 v[192:195], v129 offset:56064
	s_waitcnt lgkmcnt(0)
	s_barrier
	s_waitcnt vmcnt(9)
	ds_write_b128 v123, v[18:21] offset:35776
	s_waitcnt vmcnt(8)
	ds_write_b128 v124, v[44:47] offset:40896
	v_add_co_u32_e32 v18, vcc, s85, v22
	s_waitcnt vmcnt(7)
	ds_write_b128 v125, v[48:51] offset:46016
	s_waitcnt vmcnt(6)
	ds_write_b128 v126, v[52:55] offset:51136
	s_waitcnt vmcnt(5)
	ds_write_b128 v127, v[56:59] offset:56256
	v_addc_co_u32_e32 v19, vcc, 0, v23, vcc
	v_add_co_u32_e32 v44, vcc, s27, v22
	s_waitcnt lgkmcnt(0)
	s_nop 0
	v_addc_co_u32_e32 v45, vcc, 0, v23, vcc
	v_add_co_u32_e32 v48, vcc, s86, v22
	s_barrier
	s_nop 0
	v_addc_co_u32_e32 v49, vcc, 0, v23, vcc
	v_add_co_u32_e32 v52, vcc, s87, v22
	s_nop 1
	v_addc_co_u32_e32 v53, vcc, 0, v23, vcc
	v_add_co_u32_e32 v56, vcc, s88, v22
	global_load_dwordx4 v[18:21], v[18:19], off offset:1024
	s_nop 0
	global_load_dwordx4 v[44:47], v[44:45], off offset:2048
	s_nop 0
	global_load_dwordx4 v[48:51], v[48:49], off offset:3072
	s_nop 0
	global_load_dwordx4 v[52:55], v[52:53], off
	v_addc_co_u32_e32 v57, vcc, 0, v23, vcc
	global_load_dwordx4 v[56:59], v[56:57], off offset:1024
	v_mfma_f32_16x16x32_f16 v[14:17], v[172:175], v[156:159], v[14:17]
	v_mfma_f32_16x16x32_f16 v[2:5], v[160:163], v[60:63], v[2:5]
	v_mfma_f32_16x16x32_f16 v[6:9], v[164:167], v[60:63], v[6:9]
	v_mfma_f32_16x16x32_f16 v[10:13], v[184:187], v[60:63], v[10:13]
	v_mfma_f32_16x16x32_f16 v[14:17], v[168:171], v[60:63], v[14:17]
	v_mfma_f32_16x16x32_f16 v[2:5], v[176:179], v[152:155], v[2:5]
	v_mfma_f32_16x16x32_f16 v[6:9], v[180:183], v[152:155], v[6:9]
	v_mfma_f32_16x16x32_f16 v[10:13], v[188:191], v[152:155], v[10:13]
	v_mfma_f32_16x16x32_f16 v[14:17], v[192:195], v[152:155], v[14:17]
	ds_read_b128 v[60:63], v129 offset:35776
	ds_read_b128 v[152:155], v144 offset:1248
	ds_read_b128 v[156:159], v144 offset:1312
	ds_read_b128 v[160:163], v129 offset:35840
	s_waitcnt lgkmcnt(2)
	v_mfma_f32_16x16x32_f16 v[2:5], v[60:63], v[152:155], v[2:5]
	ds_read_b128 v[60:63], v129 offset:42432
	ds_read_b128 v[164:167], v129 offset:42496
	s_waitcnt lgkmcnt(1)
	v_mfma_f32_16x16x32_f16 v[6:9], v[60:63], v[152:155], v[6:9]
	ds_read_b128 v[60:63], v129 offset:49088
	ds_read_b128 v[168:171], v129 offset:49152
	s_waitcnt lgkmcnt(1)
	v_mfma_f32_16x16x32_f16 v[10:13], v[60:63], v[152:155], v[10:13]
	ds_read_b128 v[60:63], v129 offset:55744
	ds_read_b128 v[172:175], v129 offset:55808
	s_waitcnt lgkmcnt(1)
	v_mfma_f32_16x16x32_f16 v[14:17], v[60:63], v[152:155], v[14:17]
	ds_read_b128 v[60:63], v129 offset:35904
	v_mfma_f32_16x16x32_f16 v[2:5], v[160:163], v[156:159], v[2:5]
	v_mfma_f32_16x16x32_f16 v[6:9], v[164:167], v[156:159], v[6:9]
	v_mfma_f32_16x16x32_f16 v[10:13], v[168:171], v[156:159], v[10:13]
	s_waitcnt lgkmcnt(1)
	v_mfma_f32_16x16x32_f16 v[14:17], v[172:175], v[156:159], v[14:17]
	ds_read_b128 v[152:155], v144 offset:1376
	ds_read_b128 v[156:159], v144 offset:1440
	ds_read_b128 v[160:163], v129 offset:35968
	s_waitcnt lgkmcnt(2)
	v_mfma_f32_16x16x32_f16 v[2:5], v[60:63], v[152:155], v[2:5]
	ds_read_b128 v[60:63], v129 offset:42560
	ds_read_b128 v[164:167], v129 offset:42624
	s_waitcnt lgkmcnt(1)
	v_mfma_f32_16x16x32_f16 v[6:9], v[60:63], v[152:155], v[6:9]
	ds_read_b128 v[60:63], v129 offset:49216
	ds_read_b128 v[168:171], v129 offset:49280
	s_waitcnt lgkmcnt(1)
	v_mfma_f32_16x16x32_f16 v[10:13], v[60:63], v[152:155], v[10:13]
	ds_read_b128 v[60:63], v129 offset:55872
	ds_read_b128 v[172:175], v129 offset:55936
	s_waitcnt lgkmcnt(1)
	v_mfma_f32_16x16x32_f16 v[14:17], v[60:63], v[152:155], v[14:17]
	v_mfma_f32_16x16x32_f16 v[2:5], v[160:163], v[156:159], v[2:5]
	ds_read_b128 v[60:63], v144 offset:1504
	ds_read_b128 v[152:155], v144 offset:1568
	ds_read_b128 v[160:163], v129 offset:36032
	ds_read_b128 v[176:179], v129 offset:36096
	v_mfma_f32_16x16x32_f16 v[6:9], v[164:167], v[156:159], v[6:9]
	ds_read_b128 v[164:167], v129 offset:42688
	ds_read_b128 v[180:183], v129 offset:42752
	ds_read_b128 v[184:187], v129 offset:49344
	ds_read_b128 v[188:191], v129 offset:49408
	v_mfma_f32_16x16x32_f16 v[10:13], v[168:171], v[156:159], v[10:13]
	ds_read_b128 v[168:171], v129 offset:56000
	ds_read_b128 v[192:195], v129 offset:56064
	s_waitcnt lgkmcnt(0)
	s_barrier
	s_waitcnt vmcnt(9)
	ds_write_b128 v123, v[24:27] offset:35776
	s_waitcnt vmcnt(8)
	ds_write_b128 v124, v[28:31] offset:40896
	v_add_co_u32_e32 v24, vcc, s89, v22
	s_waitcnt vmcnt(7)
	ds_write_b128 v125, v[32:35] offset:46016
	s_waitcnt vmcnt(6)
	ds_write_b128 v126, v[36:39] offset:51136
	s_waitcnt vmcnt(5)
	ds_write_b128 v127, v[40:43] offset:56256
	v_addc_co_u32_e32 v25, vcc, 0, v23, vcc
	v_add_co_u32_e32 v28, vcc, s90, v22
	s_waitcnt lgkmcnt(0)
	s_nop 0
	v_addc_co_u32_e32 v29, vcc, 0, v23, vcc
	v_add_co_u32_e32 v32, vcc, s91, v22
	s_barrier
	s_nop 0
	v_addc_co_u32_e32 v33, vcc, 0, v23, vcc
	v_add_co_u32_e32 v36, vcc, s92, v22
	s_nop 1
	v_addc_co_u32_e32 v37, vcc, 0, v23, vcc
	v_add_co_u32_e32 v22, vcc, s93, v22
	global_load_dwordx4 v[24:27], v[24:25], off offset:2048
	s_nop 0
	global_load_dwordx4 v[28:31], v[28:29], off offset:3072
	s_nop 0
	global_load_dwordx4 v[32:35], v[32:33], off
	s_nop 0
	global_load_dwordx4 v[36:39], v[36:37], off offset:1024
	v_addc_co_u32_e32 v23, vcc, 0, v23, vcc
	global_load_dwordx4 v[40:43], v[22:23], off offset:2048
	v_mfma_f32_16x16x32_f16 v[14:17], v[172:175], v[156:159], v[14:17]
	v_mfma_f32_16x16x32_f16 v[2:5], v[160:163], v[60:63], v[2:5]
	v_mfma_f32_16x16x32_f16 v[6:9], v[164:167], v[60:63], v[6:9]
	v_mfma_f32_16x16x32_f16 v[10:13], v[184:187], v[60:63], v[10:13]
	v_mfma_f32_16x16x32_f16 v[14:17], v[168:171], v[60:63], v[14:17]
	v_mfma_f32_16x16x32_f16 v[2:5], v[176:179], v[152:155], v[2:5]
	v_mfma_f32_16x16x32_f16 v[6:9], v[180:183], v[152:155], v[6:9]
	v_mfma_f32_16x16x32_f16 v[10:13], v[188:191], v[152:155], v[10:13]
	v_mfma_f32_16x16x32_f16 v[14:17], v[192:195], v[152:155], v[14:17]
	ds_read_b128 v[60:63], v129 offset:35776
	ds_read_b128 v[152:155], v144 offset:1664
	ds_read_b128 v[156:159], v144 offset:1728
	ds_read_b128 v[160:163], v129 offset:35840
	s_waitcnt lgkmcnt(2)
	v_mfma_f32_16x16x32_f16 v[2:5], v[60:63], v[152:155], v[2:5]
	ds_read_b128 v[60:63], v129 offset:42432
	ds_read_b128 v[164:167], v129 offset:42496
	s_waitcnt lgkmcnt(1)
	v_mfma_f32_16x16x32_f16 v[6:9], v[60:63], v[152:155], v[6:9]
	ds_read_b128 v[60:63], v129 offset:49088
	ds_read_b128 v[168:171], v129 offset:49152
	s_waitcnt lgkmcnt(1)
	v_mfma_f32_16x16x32_f16 v[10:13], v[60:63], v[152:155], v[10:13]
	ds_read_b128 v[60:63], v129 offset:55744
	ds_read_b128 v[172:175], v129 offset:55808
	s_waitcnt lgkmcnt(1)
	v_mfma_f32_16x16x32_f16 v[14:17], v[60:63], v[152:155], v[14:17]
	ds_read_b128 v[60:63], v129 offset:35904
	v_mfma_f32_16x16x32_f16 v[2:5], v[160:163], v[156:159], v[2:5]
	v_mfma_f32_16x16x32_f16 v[6:9], v[164:167], v[156:159], v[6:9]
	v_mfma_f32_16x16x32_f16 v[10:13], v[168:171], v[156:159], v[10:13]
	s_waitcnt lgkmcnt(1)
	v_mfma_f32_16x16x32_f16 v[14:17], v[172:175], v[156:159], v[14:17]
	ds_read_b128 v[152:155], v144 offset:1792
	ds_read_b128 v[156:159], v144 offset:1856
	ds_read_b128 v[160:163], v129 offset:35968
	s_waitcnt lgkmcnt(2)
	v_mfma_f32_16x16x32_f16 v[2:5], v[60:63], v[152:155], v[2:5]
	ds_read_b128 v[60:63], v129 offset:42560
	ds_read_b128 v[164:167], v129 offset:42624
	s_waitcnt lgkmcnt(1)
	v_mfma_f32_16x16x32_f16 v[6:9], v[60:63], v[152:155], v[6:9]
	ds_read_b128 v[60:63], v129 offset:49216
	ds_read_b128 v[168:171], v129 offset:49280
	s_waitcnt lgkmcnt(1)
	v_mfma_f32_16x16x32_f16 v[10:13], v[60:63], v[152:155], v[10:13]
	ds_read_b128 v[60:63], v129 offset:55872
	ds_read_b128 v[172:175], v129 offset:55936
	s_waitcnt lgkmcnt(1)
	v_mfma_f32_16x16x32_f16 v[14:17], v[60:63], v[152:155], v[14:17]
	ds_read_b128 v[60:63], v129 offset:36032
	v_mfma_f32_16x16x32_f16 v[2:5], v[160:163], v[156:159], v[2:5]
	v_mfma_f32_16x16x32_f16 v[6:9], v[164:167], v[156:159], v[6:9]
	v_mfma_f32_16x16x32_f16 v[10:13], v[168:171], v[156:159], v[10:13]
	s_waitcnt lgkmcnt(1)
	v_mfma_f32_16x16x32_f16 v[14:17], v[172:175], v[156:159], v[14:17]
	ds_read_b128 v[152:155], v144 offset:1920
	ds_read_b128 v[156:159], v144 offset:1984
	ds_read_b128 v[160:163], v129 offset:36096
	s_waitcnt lgkmcnt(2)
	v_mfma_f32_16x16x32_f16 v[2:5], v[60:63], v[152:155], v[2:5]
	ds_read_b128 v[60:63], v129 offset:42688
	ds_read_b128 v[164:167], v129 offset:42752
	s_waitcnt lgkmcnt(1)
	v_mfma_f32_16x16x32_f16 v[6:9], v[60:63], v[152:155], v[6:9]
	ds_read_b128 v[60:63], v129 offset:49344
	ds_read_b128 v[168:171], v129 offset:49408
	s_waitcnt lgkmcnt(1)
	v_mfma_f32_16x16x32_f16 v[10:13], v[60:63], v[152:155], v[10:13]
	ds_read_b128 v[60:63], v129 offset:56000
	ds_read_b128 v[172:175], v129 offset:56064
	s_waitcnt lgkmcnt(0)
	s_barrier
	v_mfma_f32_16x16x32_f16 v[14:17], v[60:63], v[152:155], v[14:17]
	s_waitcnt vmcnt(9)
	ds_write_b128 v123, v[18:21] offset:35776
	s_waitcnt vmcnt(8)
	ds_write_b128 v124, v[44:47] offset:40896
	s_waitcnt vmcnt(7)
	ds_write_b128 v125, v[48:51] offset:46016
	s_waitcnt vmcnt(6)
	ds_write_b128 v126, v[52:55] offset:51136
	v_mfma_f32_16x16x32_f16 v[2:5], v[160:163], v[156:159], v[2:5]
	s_waitcnt vmcnt(5)
	ds_write_b128 v127, v[56:59] offset:56256
	s_waitcnt lgkmcnt(0)
	s_barrier
	v_mfma_f32_16x16x32_f16 v[6:9], v[164:167], v[156:159], v[6:9]
	v_mfma_f32_16x16x32_f16 v[10:13], v[168:171], v[156:159], v[10:13]
	v_mfma_f32_16x16x32_f16 v[14:17], v[172:175], v[156:159], v[14:17]
	ds_read_b128 v[18:21], v129 offset:35776
	ds_read_b128 v[44:47], v144 offset:2080
	ds_read_b128 v[48:51], v144 offset:2144
	ds_read_b128 v[52:55], v129 offset:35840
	s_waitcnt lgkmcnt(2)
	v_mfma_f32_16x16x32_f16 v[2:5], v[18:21], v[44:47], v[2:5]
	ds_read_b128 v[18:21], v129 offset:42432
	ds_read_b128 v[56:59], v129 offset:42496
	s_waitcnt lgkmcnt(1)
	v_mfma_f32_16x16x32_f16 v[6:9], v[18:21], v[44:47], v[6:9]
	ds_read_b128 v[18:21], v129 offset:49088
	ds_read_b128 v[60:63], v129 offset:49152
	s_waitcnt lgkmcnt(1)
	v_mfma_f32_16x16x32_f16 v[10:13], v[18:21], v[44:47], v[10:13]
	ds_read_b128 v[18:21], v129 offset:55744
	ds_read_b128 v[152:155], v129 offset:55808
	s_waitcnt lgkmcnt(1)
	v_mfma_f32_16x16x32_f16 v[14:17], v[18:21], v[44:47], v[14:17]
	ds_read_b128 v[18:21], v129 offset:35904
	v_mfma_f32_16x16x32_f16 v[2:5], v[52:55], v[48:51], v[2:5]
	v_mfma_f32_16x16x32_f16 v[6:9], v[56:59], v[48:51], v[6:9]
	v_mfma_f32_16x16x32_f16 v[10:13], v[60:63], v[48:51], v[10:13]
	s_waitcnt lgkmcnt(1)
	v_mfma_f32_16x16x32_f16 v[14:17], v[152:155], v[48:51], v[14:17]
	ds_read_b128 v[44:47], v144 offset:2208
	ds_read_b128 v[48:51], v144 offset:2272
	ds_read_b128 v[52:55], v129 offset:35968
	s_waitcnt lgkmcnt(2)
	v_mfma_f32_16x16x32_f16 v[2:5], v[18:21], v[44:47], v[2:5]
	ds_read_b128 v[18:21], v129 offset:42560
	ds_read_b128 v[56:59], v129 offset:42624
	s_waitcnt lgkmcnt(1)
	v_mfma_f32_16x16x32_f16 v[6:9], v[18:21], v[44:47], v[6:9]
	ds_read_b128 v[18:21], v129 offset:49216
	ds_read_b128 v[60:63], v129 offset:49280
	s_waitcnt lgkmcnt(1)
	v_mfma_f32_16x16x32_f16 v[10:13], v[18:21], v[44:47], v[10:13]
	ds_read_b128 v[18:21], v129 offset:55872
	ds_read_b128 v[152:155], v129 offset:55936
	s_waitcnt lgkmcnt(1)
	v_mfma_f32_16x16x32_f16 v[14:17], v[18:21], v[44:47], v[14:17]
	ds_read_b128 v[18:21], v129 offset:36032
	v_mfma_f32_16x16x32_f16 v[2:5], v[52:55], v[48:51], v[2:5]
	v_mfma_f32_16x16x32_f16 v[6:9], v[56:59], v[48:51], v[6:9]
	v_mfma_f32_16x16x32_f16 v[10:13], v[60:63], v[48:51], v[10:13]
	s_waitcnt lgkmcnt(1)
	v_mfma_f32_16x16x32_f16 v[14:17], v[152:155], v[48:51], v[14:17]
	ds_read_b128 v[44:47], v144 offset:2336
	ds_read_b128 v[48:51], v144 offset:2400
	ds_read_b128 v[52:55], v129 offset:36096
	s_waitcnt lgkmcnt(2)
	v_mfma_f32_16x16x32_f16 v[2:5], v[18:21], v[44:47], v[2:5]
	ds_read_b128 v[18:21], v129 offset:42688
	ds_read_b128 v[56:59], v129 offset:42752
	s_waitcnt lgkmcnt(1)
	v_mfma_f32_16x16x32_f16 v[6:9], v[18:21], v[44:47], v[6:9]
	ds_read_b128 v[18:21], v129 offset:49344
	ds_read_b128 v[60:63], v129 offset:49408
	s_waitcnt lgkmcnt(1)
	v_mfma_f32_16x16x32_f16 v[10:13], v[18:21], v[44:47], v[10:13]
	ds_read_b128 v[18:21], v129 offset:56000
	ds_read_b128 v[152:155], v129 offset:56064
	s_waitcnt lgkmcnt(0)
	s_barrier
	v_mfma_f32_16x16x32_f16 v[14:17], v[18:21], v[44:47], v[14:17]
	s_waitcnt vmcnt(4)
	ds_write_b128 v123, v[24:27] offset:35776
	s_waitcnt vmcnt(3)
	ds_write_b128 v124, v[28:31] offset:40896
	s_waitcnt vmcnt(2)
	ds_write_b128 v125, v[32:35] offset:46016
	s_waitcnt vmcnt(1)
	ds_write_b128 v126, v[36:39] offset:51136
	v_mfma_f32_16x16x32_f16 v[2:5], v[52:55], v[48:51], v[2:5]
	s_waitcnt vmcnt(0)
	ds_write_b128 v127, v[40:43] offset:56256
	s_waitcnt lgkmcnt(0)
	s_barrier
	v_mfma_f32_16x16x32_f16 v[6:9], v[56:59], v[48:51], v[6:9]
	v_mfma_f32_16x16x32_f16 v[10:13], v[60:63], v[48:51], v[10:13]
	v_mfma_f32_16x16x32_f16 v[14:17], v[152:155], v[48:51], v[14:17]
	ds_read_b128 v[18:21], v129 offset:35776
	ds_read_b128 v[22:25], v144 offset:2496
	ds_read_b128 v[26:29], v144 offset:2560
	ds_read_b128 v[30:33], v129 offset:35840
	s_waitcnt lgkmcnt(2)
	v_mfma_f32_16x16x32_f16 v[2:5], v[18:21], v[22:25], v[2:5]
	ds_read_b128 v[18:21], v129 offset:42432
	ds_read_b128 v[34:37], v129 offset:42496
	s_waitcnt lgkmcnt(1)
	v_mfma_f32_16x16x32_f16 v[6:9], v[18:21], v[22:25], v[6:9]
	ds_read_b128 v[18:21], v129 offset:49088
	ds_read_b128 v[38:41], v129 offset:49152
	s_waitcnt lgkmcnt(1)
	v_mfma_f32_16x16x32_f16 v[10:13], v[18:21], v[22:25], v[10:13]
	ds_read_b128 v[18:21], v129 offset:55744
	ds_read_b128 v[42:45], v129 offset:55808
	s_waitcnt lgkmcnt(1)
	v_mfma_f32_16x16x32_f16 v[14:17], v[18:21], v[22:25], v[14:17]
	v_mfma_f32_16x16x32_f16 v[2:5], v[30:33], v[26:29], v[2:5]
	ds_read_b128 v[18:21], v144 offset:2624
	ds_read_b128 v[22:25], v144 offset:2688
	ds_read_b128 v[30:33], v129 offset:35904
	ds_read_b128 v[46:49], v129 offset:35968
	s_waitcnt lgkmcnt(1)
	v_mfma_f32_16x16x32_f16 v[2:5], v[30:33], v[18:21], v[2:5]
	v_mfma_f32_16x16x32_f16 v[6:9], v[34:37], v[26:29], v[6:9]
	ds_read_b128 v[34:37], v129 offset:42560
	ds_read_b128 v[50:53], v129 offset:42624
	ds_read_b128 v[54:57], v129 offset:49216
	ds_read_b128 v[58:61], v129 offset:49280
	v_mfma_f32_16x16x32_f16 v[10:13], v[38:41], v[26:29], v[10:13]
	ds_read_b128 v[38:41], v129 offset:55872
	ds_read_b128 v[62:65], v129 offset:55936
	ds_read_b128 v[152:155], v129 offset:36032
	ds_read_b128 v[30:33], v144 offset:2752
	ds_read_b128 v[156:159], v144 offset:2816
	ds_read_b128 v[160:163], v129 offset:36096
	s_waitcnt lgkmcnt(10)
	v_mfma_f32_16x16x32_f16 v[2:5], v[46:49], v[22:25], v[2:5]
	ds_read_b128 v[46:49], v129 offset:42688
	ds_read_b128 v[164:167], v129 offset:42752
	ds_read_b128 v[168:171], v129 offset:49344
	ds_read_b128 v[172:175], v129 offset:49408
	s_waitcnt lgkmcnt(6)
	v_mfma_f32_16x16x32_f16 v[2:5], v[152:155], v[30:33], v[2:5]
	ds_read_b128 v[152:155], v129 offset:56000
	ds_read_b128 v[176:179], v129 offset:56064
	ds_read_b128 v[180:183], v98 offset:63808
	ds_read_b128 v[184:187], v98 offset:64064
	s_waitcnt lgkmcnt(8)
	v_mfma_f32_16x16x32_f16 v[2:5], v[160:163], v[156:159], v[2:5]
	ds_read_b128 v[160:163], v98 offset:63872
	ds_read_b128 v[188:191], v98 offset:64128
	v_mfma_f32_16x16x32_f16 v[14:17], v[42:45], v[26:29], v[14:17]
	s_waitcnt lgkmcnt(2)
	s_nop 3
	v_pk_fma_f32 v[2:3], v[2:3], v[180:181], v[184:185]
	s_nop 0
	v_pk_mul_f32 v[26:27], v[2:3], s[28:29] op_sel_hi:[1,0]
	v_mfma_f32_16x16x32_f16 v[6:9], v[34:37], v[18:21], v[6:9]
	v_mul_f32_e64 v29, |v26|, -|v26|
	v_mul_f32_e32 v29, 0x3fb8aa3b, v29
	v_fma_f32 v28, |v26|, s74, 1.0
	v_exp_f32_e32 v34, v29
	v_fma_f32 v29, |v27|, s74, 1.0
	v_rcp_f32_e32 v28, v28
	v_rcp_f32_e32 v29, v29
	v_mfma_f32_16x16x32_f16 v[10:13], v[54:57], v[18:21], v[10:13]
	v_mul_f32_e64 v35, |v27|, -|v27|
	v_mul_f32_e32 v35, 0x3fb8aa3b, v35
	v_exp_f32_e32 v35, v35
	v_mfma_f32_16x16x32_f16 v[16:19], v[38:41], v[18:21], v[14:17]
	v_mul_f32_e64 v2, v2, 0.5
	v_mul_f32_e64 v3, v3, 0.5
	s_nop 0
	v_mov_b64_e32 v[14:15], s[34:35]
	v_pk_fma_f32 v[20:21], v[28:29], s[40:41], v[14:15] op_sel_hi:[1,0,0]
	v_mfma_f32_16x16x32_f16 v[10:13], v[58:61], v[22:25], v[10:13]
	v_fma_f32 v20, v28, v20, s42
	v_fma_f32 v21, v29, v21, s42
	v_pk_fma_f32 v[20:21], v[28:29], v[20:21], s[44:45] op_sel_hi:[1,1,0]
	v_mfma_f32_16x16x32_f16 v[6:9], v[50:53], v[22:25], v[6:9]
	v_fma_f32 v20, v28, v20, s46
	v_fma_f32 v21, v29, v21, s46
	v_pk_mul_f32 v[20:21], v[20:21], v[28:29] neg_lo:[0,1] neg_hi:[0,1]
	v_mfma_f32_16x16x32_f16 v[16:19], v[62:65], v[22:25], v[16:19]
	v_fma_f32 v20, v20, v34, 1.0
	v_fma_f32 v21, v21, v35, 1.0
	v_bfi_b32 v21, s71, v21, v27
	v_bfi_b32 v20, s71, v20, v26
	v_pk_fma_f32 v[26:27], v[4:5], v[182:183], v[186:187]
	v_pk_add_f32 v[20:21], v[20:21], 1.0 op_sel_hi:[1,0]
	v_pk_mul_f32 v[28:29], v[26:27], s[28:29] op_sel_hi:[1,0]
	v_pk_mul_f32 v[24:25], v[2:3], v[20:21]
	v_mfma_f32_16x16x32_f16 v[2:5], v[168:171], v[30:33], v[10:13]
	v_mul_f32_e64 v26, v26, 0.5
	v_mul_f32_e64 v27, v27, 0.5
	s_nop 0
	v_fma_f32 v10, |v28|, s74, 1.0
	v_fma_f32 v11, |v29|, s74, 1.0
	v_rcp_f32_e32 v34, v10
	v_rcp_f32_e32 v35, v11
	v_mul_f32_e64 v10, |v28|, -|v28|
	v_mul_f32_e32 v10, 0x3fb8aa3b, v10
	v_mfma_f32_16x16x32_f16 v[6:9], v[46:49], v[30:33], v[6:9]
	v_mfma_f32_16x16x32_f16 v[16:19], v[152:155], v[30:33], v[16:19]
	v_exp_f32_e32 v30, v10
	v_mfma_f32_16x16x32_f16 v[10:13], v[172:175], v[156:159], v[2:5]
	s_nop 2
	v_mul_f32_e64 v4, |v29|, -|v29|
	v_pk_fma_f32 v[2:3], v[34:35], s[40:41], v[14:15] op_sel_hi:[1,0,0]
	v_mul_f32_e32 v4, 0x3fb8aa3b, v4
	v_pk_fma_f32 v[2:3], v[34:35], v[2:3], s[42:43] op_sel_hi:[1,1,0]
	v_exp_f32_e32 v31, v4
	v_pk_fma_f32 v[2:3], v[34:35], v[2:3], s[44:45] op_sel_hi:[1,1,0]
	v_mfma_f32_16x16x32_f16 v[20:23], v[164:167], v[156:159], v[6:9]
	v_fma_f32 v2, v34, v2, s46
	v_fma_f32 v3, v35, v3, s46
	v_pk_mul_f32 v[2:3], v[2:3], v[34:35] neg_lo:[0,1] neg_hi:[0,1]
	v_mfma_f32_16x16x32_f16 v[6:9], v[176:179], v[156:159], v[16:19]
	v_fma_f32 v2, v2, v30, 1.0
	v_fma_f32 v3, v3, v31, 1.0
	v_bfi_b32 v3, s71, v3, v29
	v_bfi_b32 v2, s71, v2, v28
	v_pk_add_f32 v[2:3], v[2:3], 1.0 op_sel_hi:[1,0]
	s_nop 0
	v_pk_mul_f32 v[4:5], v[26:27], v[2:3]
	v_cvt_pk_f16_f32 v2, v24, v25
	v_cvt_pk_f16_f32 v3, v4, v5
	s_waitcnt lgkmcnt(0)
	v_pk_fma_f32 v[4:5], v[20:21], v[160:161], v[188:189]
	s_nop 0
	v_pk_mul_f32 v[16:17], v[4:5], s[28:29] op_sel_hi:[1,0]
	v_pk_mul_f32 v[4:5], v[4:5], 0.5 op_sel_hi:[1,0]
	v_fma_f32 v18, |v16|, s74, 1.0
	v_fma_f32 v19, |v17|, s74, 1.0
	v_rcp_f32_e32 v18, v18
	v_rcp_f32_e32 v19, v19
	v_mul_f32_e64 v20, |v16|, -|v16|
	v_mul_f32_e64 v21, |v17|, -|v17|
	v_mul_f32_e32 v20, 0x3fb8aa3b, v20
	v_pk_fma_f32 v[24:25], v[18:19], s[40:41], v[14:15] op_sel_hi:[1,0,0]
	v_mul_f32_e32 v21, 0x3fb8aa3b, v21
	v_exp_f32_e32 v20, v20
	v_pk_fma_f32 v[24:25], v[18:19], v[24:25], s[42:43] op_sel_hi:[1,1,0]
	v_exp_f32_e32 v21, v21
	v_pk_fma_f32 v[24:25], v[18:19], v[24:25], s[44:45] op_sel_hi:[1,1,0]
	s_nop 0
	v_pk_fma_f32 v[24:25], v[18:19], v[24:25], s[46:47] op_sel_hi:[1,1,0]
	s_nop 0
	v_pk_mul_f32 v[18:19], v[24:25], v[18:19] neg_lo:[0,1] neg_hi:[0,1]
	s_nop 0
	v_pk_fma_f32 v[18:19], v[18:19], v[20:21], 1.0 op_sel_hi:[1,1,0]
	s_nop 0
	v_bfi_b32 v17, s71, v19, v17
	v_bfi_b32 v16, s71, v18, v16
	v_pk_add_f32 v[16:17], v[16:17], 1.0 op_sel_hi:[1,0]
	s_nop 0
	v_pk_mul_f32 v[4:5], v[4:5], v[16:17]
	v_pk_fma_f32 v[16:17], v[22:23], v[162:163], v[190:191]
	v_cvt_pk_f16_f32 v4, v4, v5
	v_pk_mul_f32 v[18:19], v[16:17], s[28:29] op_sel_hi:[1,0]
	v_pk_mul_f32 v[16:17], v[16:17], 0.5 op_sel_hi:[1,0]
	v_fma_f32 v20, |v18|, s74, 1.0
	v_fma_f32 v21, |v19|, s74, 1.0
	v_rcp_f32_e32 v20, v20
	v_rcp_f32_e32 v21, v21
	v_mul_f32_e64 v22, |v18|, -|v18|
	v_mul_f32_e64 v23, |v19|, -|v19|
	v_mul_f32_e32 v22, 0x3fb8aa3b, v22
	v_pk_fma_f32 v[24:25], v[20:21], s[40:41], v[14:15] op_sel_hi:[1,0,0]
	v_mul_f32_e32 v23, 0x3fb8aa3b, v23
	v_exp_f32_e32 v22, v22
	v_pk_fma_f32 v[24:25], v[20:21], v[24:25], s[42:43] op_sel_hi:[1,1,0]
	v_exp_f32_e32 v23, v23
	v_pk_fma_f32 v[24:25], v[20:21], v[24:25], s[44:45] op_sel_hi:[1,1,0]
	s_nop 0
	v_pk_fma_f32 v[24:25], v[20:21], v[24:25], s[46:47] op_sel_hi:[1,1,0]
	s_nop 0
	v_pk_mul_f32 v[20:21], v[24:25], v[20:21] neg_lo:[0,1] neg_hi:[0,1]
	s_nop 0
	v_pk_fma_f32 v[20:21], v[20:21], v[22:23], 1.0 op_sel_hi:[1,1,0]
	s_nop 0
	v_bfi_b32 v19, s71, v21, v19
	v_bfi_b32 v18, s71, v20, v18
	v_pk_add_f32 v[18:19], v[18:19], 1.0 op_sel_hi:[1,0]
	s_nop 0
	v_pk_mul_f32 v[16:17], v[16:17], v[18:19]
	ds_read_b128 v[18:21], v98 offset:63936
	ds_read_b128 v[22:25], v98 offset:64192
	v_cvt_pk_f16_f32 v5, v16, v17
	ds_read_b128 v[26:29], v98 offset:64000
	ds_read_b128 v[30:33], v98 offset:64256
	s_waitcnt lgkmcnt(2)
	v_pk_fma_f32 v[10:11], v[10:11], v[18:19], v[22:23]
	s_nop 0
	v_pk_mul_f32 v[22:23], v[10:11], s[28:29] op_sel_hi:[1,0]
	v_pk_fma_f32 v[12:13], v[12:13], v[20:21], v[24:25]
	v_fma_f32 v16, |v22|, s74, 1.0
	v_fma_f32 v17, |v23|, s74, 1.0
	v_rcp_f32_e32 v16, v16
	v_rcp_f32_e32 v17, v17
	v_mul_f32_e64 v18, |v22|, -|v22|
	v_mul_f32_e64 v19, |v23|, -|v23|
	v_mul_f32_e32 v18, 0x3fb8aa3b, v18
	v_pk_fma_f32 v[34:35], v[16:17], s[40:41], v[14:15] op_sel_hi:[1,0,0]
	v_mul_f32_e32 v19, 0x3fb8aa3b, v19
	v_exp_f32_e32 v18, v18
	v_pk_fma_f32 v[34:35], v[16:17], v[34:35], s[42:43] op_sel_hi:[1,1,0]
	v_exp_f32_e32 v19, v19
	v_pk_fma_f32 v[34:35], v[16:17], v[34:35], s[44:45] op_sel_hi:[1,1,0]
	v_pk_mul_f32 v[10:11], v[10:11], 0.5 op_sel_hi:[1,0]
	v_pk_fma_f32 v[34:35], v[16:17], v[34:35], s[46:47] op_sel_hi:[1,1,0]
	v_pk_mul_f32 v[20:21], v[12:13], s[28:29] op_sel_hi:[1,0]
	v_pk_mul_f32 v[16:17], v[34:35], v[16:17] neg_lo:[0,1] neg_hi:[0,1]
	v_mul_f32_e64 v24, |v20|, -|v20|
	v_pk_fma_f32 v[46:47], v[16:17], v[18:19], 1.0 op_sel_hi:[1,1,0]
	v_lshl_add_u64 v[18:19], s[50:51], 1, v[100:101]
	global_load_dwordx4 v[34:37], v[18:19], off
	global_load_dwordx4 v[42:45], v[18:19], off offset:1024
	v_lshl_add_u64 v[16:17], s[50:51], 2, v[102:103]
	global_load_dwordx4 v[38:41], v[16:17], off
	v_mov_b32_e32 v190, 0x1000
	v_mov_b32_e32 v191, 0
	global_load_dwordx4 v[152:155], v[18:19], off offset:2048
	global_load_dwordx4 v[156:159], v[18:19], off offset:3072
	global_load_dwordx4 v[160:163], v[16:17], off offset:64
	v_lshl_add_u64 v[188:189], v[18:19], 0, v[190:191]
	global_load_dwordx4 v[164:167], v[188:189], off
	global_load_dwordx4 v[168:171], v[188:189], off offset:1024
	global_load_dwordx4 v[172:175], v[16:17], off offset:128
	global_load_dwordx4 v[176:179], v[188:189], off offset:2048
	global_load_dwordx4 v[180:183], v[188:189], off offset:3072
	global_load_dwordx4 v[184:187], v[16:17], off offset:192
	v_bfi_b32 v23, s71, v47, v23
	v_bfi_b32 v22, s71, v46, v22
	v_pk_add_f32 v[22:23], v[22:23], 1.0 op_sel_hi:[1,0]
	v_mul_f32_e64 v25, |v21|, -|v21|
	v_pk_mul_f32 v[10:11], v[10:11], v[22:23]
	v_fma_f32 v22, |v20|, s74, 1.0
	v_fma_f32 v23, |v21|, s74, 1.0
	v_rcp_f32_e32 v22, v22
	v_rcp_f32_e32 v23, v23
	v_mul_f32_e32 v24, 0x3fb8aa3b, v24
	v_mul_f32_e32 v25, 0x3fb8aa3b, v25
	v_exp_f32_e32 v24, v24
	v_pk_fma_f32 v[46:47], v[22:23], s[40:41], v[14:15] op_sel_hi:[1,0,0]
	v_exp_f32_e32 v25, v25
	v_pk_fma_f32 v[46:47], v[22:23], v[46:47], s[42:43] op_sel_hi:[1,1,0]
	v_pk_mul_f32 v[12:13], v[12:13], 0.5 op_sel_hi:[1,0]
	v_pk_fma_f32 v[46:47], v[22:23], v[46:47], s[44:45] op_sel_hi:[1,1,0]
	s_waitcnt lgkmcnt(0)
	v_pk_fma_f32 v[6:7], v[6:7], v[26:27], v[30:31]
	v_pk_fma_f32 v[46:47], v[22:23], v[46:47], s[46:47] op_sel_hi:[1,1,0]
	v_cvt_pk_f16_f32 v10, v10, v11
	v_pk_mul_f32 v[22:23], v[46:47], v[22:23] neg_lo:[0,1] neg_hi:[0,1]
	v_pk_fma_f32 v[8:9], v[8:9], v[28:29], v[32:33]
	v_pk_fma_f32 v[22:23], v[22:23], v[24:25], 1.0 op_sel_hi:[1,1,0]
	s_mul_i32 s50, s94, 0xfef85000
	v_bfi_b32 v21, s71, v23, v21
	v_bfi_b32 v20, s71, v22, v20
	v_pk_add_f32 v[20:21], v[20:21], 1.0 op_sel_hi:[1,0]
	s_nop 0
	v_pk_mul_f32 v[12:13], v[12:13], v[20:21]
	s_nop 0
	v_cvt_pk_f16_f32 v11, v12, v13
	v_pk_mul_f32 v[12:13], v[6:7], s[28:29] op_sel_hi:[1,0]
	v_pk_mul_f32 v[6:7], v[6:7], 0.5 op_sel_hi:[1,0]
	v_fma_f32 v20, |v12|, s74, 1.0
	v_fma_f32 v21, |v13|, s74, 1.0
	v_rcp_f32_e32 v20, v20
	v_rcp_f32_e32 v21, v21
	v_mul_f32_e64 v22, |v12|, -|v12|
	v_mul_f32_e64 v23, |v13|, -|v13|
	v_mul_f32_e32 v22, 0x3fb8aa3b, v22
	v_pk_fma_f32 v[24:25], v[20:21], s[40:41], v[14:15] op_sel_hi:[1,0,0]
	v_mul_f32_e32 v23, 0x3fb8aa3b, v23
	v_exp_f32_e32 v22, v22
	v_pk_fma_f32 v[24:25], v[20:21], v[24:25], s[42:43] op_sel_hi:[1,1,0]
	v_exp_f32_e32 v23, v23
	v_pk_fma_f32 v[24:25], v[20:21], v[24:25], s[44:45] op_sel_hi:[1,1,0]
	s_nop 0
	v_pk_fma_f32 v[24:25], v[20:21], v[24:25], s[46:47] op_sel_hi:[1,1,0]
	s_nop 0
	v_pk_mul_f32 v[20:21], v[24:25], v[20:21] neg_lo:[0,1] neg_hi:[0,1]
	s_nop 0
	v_pk_fma_f32 v[20:21], v[20:21], v[22:23], 1.0 op_sel_hi:[1,1,0]
	s_nop 0
	v_bfi_b32 v13, s71, v21, v13
	v_bfi_b32 v12, s71, v20, v12
	v_pk_add_f32 v[12:13], v[12:13], 1.0 op_sel_hi:[1,0]
	s_nop 0
	v_pk_mul_f32 v[6:7], v[6:7], v[12:13]
	v_pk_mul_f32 v[12:13], v[8:9], s[28:29] op_sel_hi:[1,0]
	v_pk_mul_f32 v[8:9], v[8:9], 0.5 op_sel_hi:[1,0]
	v_fma_f32 v20, |v12|, s74, 1.0
	v_fma_f32 v21, |v13|, s74, 1.0
	v_rcp_f32_e32 v20, v20
	v_rcp_f32_e32 v21, v21
	v_mul_f32_e64 v22, |v12|, -|v12|
	v_mul_f32_e64 v23, |v13|, -|v13|
	v_mul_f32_e32 v22, 0x3fb8aa3b, v22
	v_pk_fma_f32 v[14:15], v[20:21], s[40:41], v[14:15] op_sel_hi:[1,0,0]
	v_mul_f32_e32 v23, 0x3fb8aa3b, v23
	v_exp_f32_e32 v22, v22
	v_pk_fma_f32 v[14:15], v[20:21], v[14:15], s[42:43] op_sel_hi:[1,1,0]
	v_exp_f32_e32 v23, v23
	v_pk_fma_f32 v[14:15], v[20:21], v[14:15], s[44:45] op_sel_hi:[1,1,0]
	s_nop 0
	v_pk_fma_f32 v[14:15], v[20:21], v[14:15], s[46:47] op_sel_hi:[1,1,0]
	s_nop 0
	v_pk_mul_f32 v[14:15], v[14:15], v[20:21] neg_lo:[0,1] neg_hi:[0,1]
	s_nop 0
	v_pk_fma_f32 v[14:15], v[14:15], v[22:23], 1.0 op_sel_hi:[1,1,0]
	s_nop 0
	v_bfi_b32 v13, s71, v15, v13
	v_bfi_b32 v12, s71, v14, v12
	v_pk_add_f32 v[12:13], v[12:13], 1.0 op_sel_hi:[1,0]
	v_add_u32_e32 v14, s95, v128
	v_pk_mul_f32 v[8:9], v[8:9], v[12:13]
	v_cvt_pk_f16_f32 v12, v6, v7
	v_cvt_pk_f16_f32 v13, v8, v9
	s_waitcnt vmcnt(0)
	v_pk_mul_f32 v[8:9], v[40:41], s[48:49] op_sel_hi:[1,0]
	v_pk_mul_f32 v[6:7], v[38:39], s[48:49] op_sel_hi:[1,0]
	v_cmp_gt_i32_e64 s[20:21], s73, v14
	v_add_u32_e32 v14, s50, v134
	v_mfma_f32_16x16x32_f16 v[6:9], v[34:37], v[2:5], v[6:9]
	v_mfma_f32_16x16x32_f16 v[6:9], v[42:45], v[10:13], v[6:9]
	v_pk_mul_f32 v[160:161], v[160:161], s[48:49] op_sel_hi:[1,0]
	v_pk_mul_f32 v[162:163], v[162:163], s[48:49] op_sel_hi:[1,0]
	v_pk_mul_f32 v[172:173], v[172:173], s[48:49] op_sel_hi:[1,0]
	v_pk_mul_f32 v[174:175], v[174:175], s[48:49] op_sel_hi:[1,0]
	v_pk_mul_f32 v[184:185], v[184:185], s[48:49] op_sel_hi:[1,0]
	v_pk_mul_f32 v[186:187], v[186:187], s[48:49] op_sel_hi:[1,0]
	s_nop 1
	v_mfma_f32_16x16x32_f16 v[20:23], v[152:155], v[2:5], v[160:163]
	v_mfma_f32_16x16x32_f16 v[24:27], v[164:167], v[2:5], v[172:175]
	v_mfma_f32_16x16x32_f16 v[28:31], v[176:179], v[2:5], v[184:187]
	v_mfma_f32_16x16x32_f16 v[20:23], v[156:159], v[10:13], v[20:23]
	v_mfma_f32_16x16x32_f16 v[24:27], v[168:171], v[10:13], v[24:27]
	v_mfma_f32_16x16x32_f16 v[28:31], v[180:183], v[10:13], v[28:31]
	s_and_saveexec_b64 s[50:51], s[20:21]
	s_cbranch_execz .Lmy_k2_nostore
	s_nop 7
	buffer_store_dwordx4 v[6:9], v14, s[24:27], 0 offen sc1
	buffer_store_dwordx4 v[20:23], v14, s[24:27], 0 offen offset:64 sc1
	buffer_store_dwordx4 v[24:27], v14, s[24:27], 0 offen offset:128 sc1
	buffer_store_dwordx4 v[28:31], v14, s[24:27], 0 offen offset:192 sc1
.Lmy_k2_nostore:
.LBB3_20:
	s_or_b64 exec, exec, s[50:51]
	s_waitcnt vmcnt(0)
	s_barrier
	s_and_saveexec_b64 s[20:21], s[18:19]
	s_cbranch_execz .LBB3_3
	s_lshl_b32 s50, s94, 6
	s_ashr_i32 s51, s50, 31
	s_sub_i32 s56, s3, s50
	s_lshl_b64 s[50:51], s[50:51], 2
	s_add_u32 s58, s54, s50
	s_addc_u32 s59, s55, s51
	s_ashr_i32 s57, s56, 31
	s_lshl_b64 s[50:51], s[56:57], 2
	s_add_u32 s50, s58, s50
	s_addc_u32 s51, s59, s51
	global_store_dword v67, v145, s[50:51] sc1
	s_branch .LBB3_3

.LBB3_166:
	s_waitcnt lgkmcnt(0)
	s_andn2_saveexec_b64 s[8:9], s[38:39]
	s_cbranch_execz .LBB3_175
	s_load_dwordx4 s[4:7], s[0:1], 0xa8
	s_load_dwordx2 s[2:3], s[0:1], 0xb8
	v_lshrrev_b32_e32 v29, 2, v0
	v_lshlrev_b32_e32 v49, 6, v0
	v_and_b32_e32 v41, 12, v29
	v_and_b32_e32 v45, 0x3c0, v49
	v_or_b32_e32 v53, 3, v29
	v_or_b32_e32 v2, v41, v45
	v_or_b32_e32 v5, v53, v45
	v_lshlrev_b32_e32 v21, 2, v2
	v_lshlrev_b32_e32 v13, 2, v5
	v_or_b32_e32 v89, 19, v29
	s_waitcnt lgkmcnt(0)
	global_load_dwordx3 v[2:4], v21, s[4:5]
	global_load_dwordx3 v[6:8], v21, s[6:7]
	global_load_dword v5, v13, s[4:5]
	global_load_dword v9, v13, s[6:7]
	global_load_dwordx3 v[10:12], v21, s[4:5] offset:64
	global_load_dwordx3 v[14:16], v21, s[6:7] offset:64
	v_or_b32_e32 v13, v89, v45
	v_lshlrev_b32_e32 v25, 2, v13
	v_or_b32_e32 v93, 35, v29
	v_or_b32_e32 v61, 0x400, v45
	global_load_dword v13, v25, s[4:5]
	global_load_dword v17, v25, s[6:7]
	global_load_dwordx3 v[18:20], v21, s[4:5] offset:128
	global_load_dwordx3 v[22:24], v21, s[6:7] offset:128
	v_or_b32_e32 v25, v93, v45
	global_load_dwordx3 v[26:28], v21, s[4:5] offset:192
	global_load_dwordx3 v[30:32], v21, s[6:7] offset:192
	v_or_b32_e32 v21, v61, v41
	v_lshlrev_b32_e32 v62, 2, v21
	v_lshlrev_b32_e32 v33, 2, v25
	global_load_dwordx3 v[34:36], v62, s[4:5] offset:64
	global_load_dwordx3 v[42:44], v62, s[6:7] offset:64
	global_load_dword v21, v33, s[4:5]
	global_load_dword v25, v33, s[6:7]
	v_or_b32_e32 v81, 51, v29
	v_or_b32_e32 v29, v81, v45
	v_lshlrev_b32_e32 v37, 2, v29
	global_load_dword v29, v37, s[4:5]
	global_load_dword v33, v37, s[6:7]
	v_or_b32_e32 v37, v61, v89
	v_lshlrev_b32_e32 v38, 2, v37
	global_load_dword v37, v38, s[4:5]
	global_load_dword v39, v38, s[6:7]
	global_load_dwordx3 v[46:48], v62, s[4:5] offset:128
	global_load_dwordx3 v[50:52], v62, s[6:7] offset:128
	v_or_b32_e32 v38, v61, v93
	v_lshlrev_b32_e32 v38, 2, v38
	global_load_dword v63, v38, s[4:5]
	global_load_dword v95, v38, s[6:7]
	global_load_dwordx3 v[54:56], v62, s[4:5] offset:192
	global_load_dwordx3 v[58:60], v62, s[6:7] offset:192
	s_mov_b32 s0, 0x4038aa3b
	s_mov_b32 s10, 0x3f2aaaab
	s_mov_b32 s11, 0x3f317218
	v_or_b32_e32 v40, s34, v65
	v_lshlrev_b32_e32 v118, 6, v64
	v_lshlrev_b32_e32 v65, 7, v65
	s_waitcnt vmcnt(24)
	v_pk_mul_f32 v[2:3], v[2:3], v[6:7]
	s_waitcnt vmcnt(20)
	v_pk_mul_f32 v[6:7], v[10:11], v[14:15]
	v_pk_mul_f32 v[4:5], v[4:5], v[8:9]
	v_pk_mul_f32 v[6:7], v[6:7], s[0:1] op_sel_hi:[1,0]
	s_waitcnt vmcnt(18)
	v_pk_mul_f32 v[8:9], v[12:13], v[16:17]
	v_pk_mul_f32 v[2:3], v[2:3], s[0:1] op_sel_hi:[1,0]
	s_waitcnt vmcnt(16)
	v_pk_mul_f32 v[10:11], v[18:19], v[22:23]
	v_pk_mul_f32 v[22:23], v[8:9], s[0:1] op_sel_hi:[1,0]
	v_pk_mul_f32 v[10:11], v[10:11], s[0:1] op_sel_hi:[1,0]
	s_waitcnt vmcnt(14)
	v_pk_mul_f32 v[14:15], v[26:27], v[30:31]
	v_cvt_pk_f16_f32 v2, v2, v3
	v_pk_mul_f32 v[14:15], v[14:15], s[0:1] op_sel_hi:[1,0]
	s_waitcnt vmcnt(12)
	v_pk_mul_f32 v[18:19], v[34:35], v[42:43]
	s_waitcnt vmcnt(10)
	v_pk_mul_f32 v[12:13], v[20:21], v[24:25]
	v_pk_mul_f32 v[20:21], v[4:5], s[0:1] op_sel_hi:[1,0]
	v_cvt_pk_f16_f32 v4, v6, v7
	v_cvt_pk_f16_f32 v6, v10, v11
	v_pk_mul_f32 v[10:11], v[12:13], s[0:1] op_sel_hi:[1,0]
	s_waitcnt vmcnt(8)
	v_pk_mul_f32 v[16:17], v[28:29], v[32:33]
	v_cvt_pk_f16_f32 v7, v10, v11
	v_or_b32_e32 v10, v61, v81
	v_or_b32_e32 v11, v61, v53
	v_pk_mul_f32 v[18:19], v[18:19], s[0:1] op_sel_hi:[1,0]
	v_cvt_pk_f16_f32 v8, v14, v15
	v_lshlrev_b32_e32 v10, 2, v10
	v_lshlrev_b32_e32 v11, 2, v11
	v_or_b32_e32 v14, 0x800, v45
	v_pk_mul_f32 v[12:13], v[16:17], s[0:1] op_sel_hi:[1,0]
	v_cvt_pk_f16_f32 v3, v20, v21
	v_cvt_pk_f16_f32 v5, v22, v23
	global_load_dword v33, v10, s[4:5]
	global_load_dword v57, v10, s[6:7]
	v_cvt_pk_f16_f32 v10, v18, v19
	v_mov_b32_e32 v38, v44
	global_load_dwordx3 v[16:18], v62, s[4:5]
	global_load_dwordx3 v[20:22], v62, s[6:7]
	global_load_dword v19, v11, s[4:5]
	global_load_dword v23, v11, s[6:7]
	v_or_b32_e32 v11, v14, v41
	v_cvt_pk_f16_f32 v9, v12, v13
	s_waitcnt vmcnt(12)
	v_pk_mul_f32 v[12:13], v[36:37], v[38:39]
	v_lshlrev_b32_e32 v15, 2, v11
	v_or_b32_e32 v11, v14, v93
	v_pk_mul_f32 v[12:13], v[12:13], s[0:1] op_sel_hi:[1,0]
	v_lshlrev_b32_e32 v11, 2, v11
	global_load_dwordx3 v[24:26], v15, s[4:5] offset:128
	global_load_dwordx3 v[28:30], v15, s[6:7] offset:128
	global_load_dword v27, v11, s[4:5]
	global_load_dword v31, v11, s[6:7]
	v_cvt_pk_f16_f32 v11, v12, v13
	s_waitcnt vmcnt(14)
	v_pk_mul_f32 v[12:13], v[46:47], v[50:51]
	v_or_b32_e32 v32, v14, v81
	v_pk_mul_f32 v[12:13], v[12:13], s[0:1] op_sel_hi:[1,0]
	global_load_dwordx3 v[42:44], v15, s[4:5] offset:192
	global_load_dwordx3 v[66:68], v15, s[6:7] offset:192
	v_lshlrev_b32_e32 v32, 2, v32
	v_cvt_pk_f16_f32 v12, v12, v13
	v_or_b32_e32 v13, v14, v53
	global_load_dword v39, v32, s[4:5]
	global_load_dword v45, v32, s[6:7]
	v_lshlrev_b32_e32 v13, 2, v13
	global_load_dwordx3 v[70:72], v15, s[4:5]
	global_load_dwordx3 v[74:76], v15, s[6:7]
	global_load_dword v61, v13, s[4:5]
	global_load_dword v69, v13, s[6:7]
	global_load_dwordx3 v[78:80], v15, s[4:5] offset:64
	global_load_dwordx3 v[82:84], v15, s[6:7] offset:64
	v_or_b32_e32 v13, v14, v89
	v_lshlrev_b32_e32 v13, 2, v13
	v_or_b32_e32 v38, 0xc00, v49
	global_load_dword v73, v13, s[4:5]
	global_load_dword v77, v13, s[6:7]
	v_or_b32_e32 v13, v41, v38
	v_lshlrev_b32_e32 v32, 2, v13
	v_or_b32_e32 v13, v81, v38
	global_load_dwordx3 v[86:88], v32, s[4:5] offset:192
	global_load_dwordx3 v[90:92], v32, s[6:7] offset:192
	v_mov_b32_e32 v62, v48
	v_lshlrev_b32_e32 v13, 2, v13
	v_mov_b32_e32 v94, v52
	global_load_dword v81, v13, s[4:5]
	global_load_dword v85, v13, s[6:7]
	s_waitcnt vmcnt(28)
	v_pk_mul_f32 v[14:15], v[62:63], v[94:95]
	v_or_b32_e32 v13, v53, v38
	v_lshlrev_b32_e32 v13, 2, v13
	v_pk_mul_f32 v[14:15], v[14:15], s[0:1] op_sel_hi:[1,0]
	global_load_dwordx3 v[46:48], v32, s[4:5]
	global_load_dwordx3 v[50:52], v32, s[6:7]
	global_load_dword v49, v13, s[4:5]
	global_load_dword v53, v13, s[6:7]
	v_cvt_pk_f16_f32 v13, v14, v15
	v_or_b32_e32 v14, v89, v38
	global_load_dwordx3 v[94:96], v32, s[4:5] offset:64
	global_load_dwordx3 v[98:100], v32, s[6:7] offset:64
	v_lshlrev_b32_e32 v14, 2, v14
	global_load_dword v63, v14, s[4:5]
	global_load_dword v89, v14, s[6:7]
	global_load_dwordx3 v[102:104], v32, s[4:5] offset:128
	global_load_dwordx3 v[106:108], v32, s[6:7] offset:128
	v_lshlrev_b32_e32 v32, 4, v0
	v_and_or_b32 v32, v32, 48, v41
	v_lshlrev_b32_e32 v32, 2, v32
	global_load_dwordx4 v[34:37], v32, s[2:3]
	s_waitcnt vmcnt(37)
	v_pk_mul_f32 v[14:15], v[54:55], v[58:59]
	v_mov_b32_e32 v32, v56
	v_pk_mul_f32 v[14:15], v[14:15], s[0:1] op_sel_hi:[1,0]
	v_mov_b32_e32 v56, v60
	v_cvt_pk_f16_f32 v14, v14, v15
	v_or_b32_e32 v15, v93, v38
	v_lshlrev_b32_e32 v15, 2, v15
	s_mov_b32 s2, 0xc2ce8ed0
	s_mov_b32 s3, 0x42b17218
	v_and_b32_e32 v0, 48, v0
	s_waitcnt vmcnt(35)
	v_pk_mul_f32 v[32:33], v[32:33], v[56:57]
	global_load_dword v55, v15, s[4:5]
	global_load_dword v57, v15, s[6:7]
	v_pk_mul_f32 v[32:33], v[32:33], s[0:1] op_sel_hi:[1,0]
	s_waitcnt vmcnt(35)
	v_pk_mul_f32 v[16:17], v[16:17], v[20:21]
	s_waitcnt vmcnt(33)
	v_pk_mul_f32 v[18:19], v[18:19], v[22:23]
	v_pk_mul_f32 v[16:17], v[16:17], s[0:1] op_sel_hi:[1,0]
	v_pk_mul_f32 v[18:19], v[18:19], s[0:1] op_sel_hi:[1,0]
	v_cvt_pk_f16_f32 v16, v16, v17
	v_cvt_pk_f16_f32 v17, v18, v19
	v_cvt_pk_f16_f32 v15, v32, v33
	s_mov_b32 s4, 0x7f800000
	s_mov_b32 s6, 0x33800000
	s_waitcnt vmcnt(31)
	v_pk_mul_f32 v[18:19], v[24:25], v[28:29]
	s_waitcnt vmcnt(29)
	v_pk_mul_f32 v[20:21], v[26:27], v[30:31]
	v_pk_mul_f32 v[18:19], v[18:19], s[0:1] op_sel_hi:[1,0]
	v_pk_mul_f32 v[20:21], v[20:21], s[0:1] op_sel_hi:[1,0]
	v_cvt_pk_f16_f32 v18, v18, v19
	s_waitcnt vmcnt(28)
	v_mov_b32_e32 v38, v44
	s_waitcnt vmcnt(27)
	v_mov_b32_e32 v44, v68
	v_cvt_pk_f16_f32 v19, v20, v21
	v_pk_mul_f32 v[20:21], v[42:43], v[66:67]
	s_mov_b32 s7, 0x3c23d70a
	s_waitcnt vmcnt(25)
	v_pk_mul_f32 v[22:23], v[38:39], v[44:45]
	v_pk_mul_f32 v[20:21], v[20:21], s[0:1] op_sel_hi:[1,0]
	v_pk_mul_f32 v[22:23], v[22:23], s[0:1] op_sel_hi:[1,0]
	s_waitcnt vmcnt(24)
	v_mov_b32_e32 v60, v72
	s_waitcnt vmcnt(23)
	v_mov_b32_e32 v68, v76
	v_cvt_pk_f16_f32 v20, v20, v21
	v_cvt_pk_f16_f32 v21, v22, v23
	v_pk_mul_f32 v[22:23], v[70:71], v[74:75]
	s_waitcnt vmcnt(21)
	v_pk_mul_f32 v[24:25], v[60:61], v[68:69]
	v_pk_mul_f32 v[22:23], v[22:23], s[0:1] op_sel_hi:[1,0]
	v_pk_mul_f32 v[24:25], v[24:25], s[0:1] op_sel_hi:[1,0]
	s_waitcnt vmcnt(20)
	v_mov_b32_e32 v72, v80
	s_waitcnt vmcnt(19)
	v_mov_b32_e32 v76, v84
	v_cvt_pk_f16_f32 v22, v22, v23
	v_cvt_pk_f16_f32 v23, v24, v25
	v_pk_mul_f32 v[24:25], v[78:79], v[82:83]
	s_waitcnt vmcnt(17)
	v_pk_mul_f32 v[26:27], v[72:73], v[76:77]
	v_pk_mul_f32 v[24:25], v[24:25], s[0:1] op_sel_hi:[1,0]
	v_pk_mul_f32 v[26:27], v[26:27], s[0:1] op_sel_hi:[1,0]
	s_waitcnt vmcnt(16)
	v_mov_b32_e32 v80, v88
	s_waitcnt vmcnt(15)
	v_mov_b32_e32 v84, v92
	v_cvt_pk_f16_f32 v24, v24, v25
	v_cvt_pk_f16_f32 v25, v26, v27
	v_pk_mul_f32 v[26:27], v[86:87], v[90:91]
	s_waitcnt vmcnt(13)
	v_pk_mul_f32 v[28:29], v[80:81], v[84:85]
	v_pk_mul_f32 v[26:27], v[26:27], s[0:1] op_sel_hi:[1,0]
	v_pk_mul_f32 v[28:29], v[28:29], s[0:1] op_sel_hi:[1,0]
	v_cvt_pk_f16_f32 v26, v26, v27
	v_cvt_pk_f16_f32 v27, v28, v29
	s_waitcnt vmcnt(11)
	v_pk_mul_f32 v[28:29], v[46:47], v[50:51]
	s_waitcnt vmcnt(9)
	v_pk_mul_f32 v[30:31], v[48:49], v[52:53]
	v_pk_mul_f32 v[28:29], v[28:29], s[0:1] op_sel_hi:[1,0]
	v_pk_mul_f32 v[30:31], v[30:31], s[0:1] op_sel_hi:[1,0]
	s_waitcnt vmcnt(8)
	v_mov_b32_e32 v62, v96
	s_waitcnt vmcnt(7)
	v_mov_b32_e32 v88, v100
	v_cvt_pk_f16_f32 v28, v28, v29
	v_cvt_pk_f16_f32 v29, v30, v31
	v_pk_mul_f32 v[30:31], v[94:95], v[98:99]
	s_waitcnt vmcnt(5)
	v_pk_mul_f32 v[32:33], v[62:63], v[88:89]
	v_pk_mul_f32 v[30:31], v[30:31], s[0:1] op_sel_hi:[1,0]
	v_pk_mul_f32 v[32:33], v[32:33], s[0:1] op_sel_hi:[1,0]
	v_cvt_pk_f16_f32 v30, v30, v31
	v_cvt_pk_f16_f32 v31, v32, v33
	s_waitcnt vmcnt(3)
	v_pk_mul_f32 v[32:33], v[102:103], v[106:107]
	s_waitcnt vmcnt(2)
	v_cmp_ngt_f32_e32 vcc, s2, v34
	v_pk_mul_f32 v[32:33], v[32:33], s[0:1] op_sel_hi:[1,0]
	s_mov_b32 s1, 0x3fb8aa3b
	v_cvt_pk_f16_f32 v32, v32, v33
	v_mul_f32_e32 v33, 0x3fb8aa3b, v34
	v_fma_f32 v38, v34, s1, -v33
	v_rndne_f32_e32 v39, v33
	v_fmac_f32_e32 v38, 0x32a5705f, v34
	v_sub_f32_e32 v33, v33, v39
	v_add_f32_e32 v33, v33, v38
	v_exp_f32_e32 v33, v33
	v_cvt_i32_f32_e32 v38, v39
	v_mov_b32_e32 v107, 0x7f800000
	v_mov_b32_e32 v54, v104
	v_mov_b32_e32 v56, v108
	v_ldexp_f32 v33, v33, v38
	v_cndmask_b32_e32 v33, 0, v33, vcc
	v_cmp_nlt_f32_e32 vcc, s3, v34
	s_waitcnt vmcnt(0)
	v_pk_mul_f32 v[42:43], v[54:55], v[56:57]
	v_mov_b32_e32 v103, 0x41200000
	v_cndmask_b32_e32 v33, v107, v33, vcc
	v_add_f32_e32 v34, 1.0, v33
	v_add_f32_e32 v38, -1.0, v34
	v_sub_f32_e32 v39, v38, v34
	v_add_f32_e32 v39, 1.0, v39
	v_sub_f32_e32 v38, v33, v38
	v_add_f32_e32 v41, v38, v39
	v_frexp_mant_f32_e32 v44, v34
	v_cvt_f64_f32_e32 v[38:39], v34
	v_frexp_exp_i32_f64_e32 v38, v[38:39]
	v_cmp_gt_f32_e32 vcc, s10, v44
	s_mov_b32 s5, 0xbd23d70a
	v_pk_mul_f32 v[42:43], v[42:43], s[0:1] op_sel_hi:[1,0]
	v_subbrev_co_u32_e32 v50, vcc, 0, v38, vcc
	v_sub_u32_e32 v38, 0, v50
	v_ldexp_f32 v34, v34, v38
	v_ldexp_f32 v38, v41, v38
	v_add_f32_e32 v41, -1.0, v34
	v_add_f32_e32 v39, 1.0, v41
	v_sub_f32_e32 v39, v34, v39
	v_add_f32_e32 v44, v38, v39
	v_add_f32_e32 v39, 1.0, v34
	v_add_f32_e32 v45, -1.0, v39
	v_sub_f32_e32 v34, v34, v45
	v_add_f32_e32 v34, v38, v34
	v_add_f32_e32 v51, v39, v34
	v_rcp_f32_e32 v52, v51
	v_sub_f32_e32 v38, v39, v51
	v_add_f32_e32 v39, v41, v44
	v_add_f32_e32 v34, v34, v38
	v_sub_f32_e32 v38, v41, v39
	v_mul_f32_e32 v53, v39, v52
	v_add_f32_e32 v41, v44, v38
	v_mul_f32_e32 v44, v51, v53
	v_fma_f32 v46, v53, v51, -v44
	v_fmac_f32_e32 v46, v53, v34
	v_add_f32_e32 v38, v44, v46
	v_sub_f32_e32 v45, v39, v38
	v_pk_add_f32 v[48:49], v[38:39], v[44:45] neg_lo:[0,1] neg_hi:[0,1]
	v_mov_b32_e32 v47, v38
	v_pk_add_f32 v[38:39], v[48:49], v[46:47] neg_lo:[0,1] neg_hi:[0,1]
	v_cmp_neq_f32_e32 vcc, s4, v33
	v_add_f32_e32 v39, v41, v39
	v_add_f32_e32 v38, v38, v39
	v_add_f32_e32 v39, v45, v38
	v_mul_f32_e32 v41, v52, v39
	v_mul_f32_e32 v44, v51, v41
	v_fma_f32 v46, v41, v51, -v44
	v_fmac_f32_e32 v46, v41, v34
	v_sub_f32_e32 v34, v45, v39
	v_add_f32_e32 v34, v38, v34
	v_add_f32_e32 v38, v44, v46
	v_sub_f32_e32 v45, v39, v38
	v_pk_add_f32 v[48:49], v[38:39], v[44:45] neg_lo:[0,1] neg_hi:[0,1]
	v_mov_b32_e32 v47, v38
	v_pk_add_f32 v[38:39], v[48:49], v[46:47] neg_lo:[0,1] neg_hi:[0,1]
	v_cvt_f32_i32_e32 v44, v50
	v_add_f32_e32 v34, v34, v39
	v_add_f32_e32 v34, v38, v34
	v_add_f32_e32 v38, v53, v41
	v_add_f32_e32 v34, v45, v34
	v_sub_f32_e32 v39, v38, v53
	v_mul_f32_e32 v34, v52, v34
	v_sub_f32_e32 v39, v41, v39
	v_add_f32_e32 v41, v39, v34
	v_add_f32_e32 v45, v38, v41
	v_mul_f32_e32 v46, v45, v45
	v_mov_b32_e32 v34, 0x3ecc95a3
	v_sub_f32_e32 v38, v45, v38
	v_fmamk_f32 v39, v46, 0x3e9b6dac, v34
	v_sub_f32_e32 v38, v41, v38
	v_fmaak_f32 v39, v46, v39, 0x3f2aaada
	v_ldexp_f32 v47, v45, 1
	v_ldexp_f32 v41, v38, 1
	v_mul_f32_e32 v45, v45, v46
	v_mov_b32_e32 v38, 0x3f317218
	v_pk_mul_f32 v[48:49], v[44:45], v[38:39]
	s_mov_b32 s0, 0x42000
	v_fma_f32 v46, v44, s11, -v48
	v_fmac_f32_e32 v46, 0xb102e308, v44
	v_pk_add_f32 v[44:45], v[48:49], v[46:47]
	v_mov_b32_e32 v50, v48
	v_sub_f32_e32 v39, v45, v47
	v_sub_f32_e32 v39, v49, v39
	v_add_f32_e32 v51, v41, v39
	v_pk_add_f32 v[48:49], v[44:45], v[48:49] neg_lo:[0,1] neg_hi:[0,1]
	v_pk_add_f32 v[52:53], v[44:45], v[50:51]
	v_mov_b32_e32 v47, v44
	v_mov_b32_e32 v49, v53
	v_pk_add_f32 v[54:55], v[46:47], v[48:49] neg_lo:[0,1] neg_hi:[0,1]
	v_pk_add_f32 v[46:47], v[46:47], v[48:49]
	v_mov_b32_e32 v50, v51
	v_pk_add_f32 v[48:49], v[46:47], v[44:45] op_sel:[1,0] op_sel_hi:[0,1] neg_lo:[0,1] neg_hi:[0,1]
	v_pk_add_f32 v[56:57], v[52:53], v[48:49] op_sel_hi:[1,0] neg_lo:[0,1] neg_hi:[0,1]
	v_mov_b32_e32 v52, v53
	v_mov_b32_e32 v53, v47
	v_pk_mov_b32 v[48:49], v[44:45], v[48:49] op_sel:[1,0]
	v_mov_b32_e32 v51, v44
	v_pk_add_f32 v[48:49], v[52:53], v[48:49] neg_lo:[0,1] neg_hi:[0,1]
	v_mov_b32_e32 v56, v54
	v_pk_add_f32 v[44:45], v[50:51], v[48:49] neg_lo:[0,1] neg_hi:[0,1]
	v_mov_b32_e32 v55, v47
	v_pk_add_f32 v[48:49], v[56:57], v[44:45]
	v_mov_b32_e32 v56, 0x3f2aaada
	v_pk_add_f32 v[50:51], v[48:49], v[48:49] op_sel:[0,1] op_sel_hi:[1,0]
	v_mov_b32_e32 v63, 0
	v_pk_add_f32 v[46:47], v[46:47], v[50:51] op_sel:[1,0] op_sel_hi:[0,1]
	v_mov_b32_e32 v49, v46
	v_pk_add_f32 v[52:53], v[48:49], v[54:55] neg_lo:[0,1] neg_hi:[0,1]
	v_mov_b32_e32 v45, v50
	v_sub_f32_e32 v39, v48, v52
	v_pk_add_f32 v[44:45], v[44:45], v[52:53] neg_lo:[0,1] neg_hi:[0,1]
	v_sub_f32_e32 v39, v54, v39
	v_add_f32_e32 v39, v44, v39
	v_add_f32_e32 v39, v39, v45
	v_add_f32_e32 v39, v46, v39
	v_cndmask_b32_e32 v39, v107, v39, vcc
	v_cmp_lt_f32_e64 vcc, |v33|, s6
	v_mul_lo_u32 v62, v40, s0
	v_mov_b32_e32 v119, v63
	v_cndmask_b32_e32 v33, v39, v33, vcc
	v_add_f32_e32 v33, 0x358637bd, v33
	v_med3_f32 v39, v33, s7, v103
	v_div_scale_f32 v41, s[12:13], v39, v39, s5
	v_rcp_f32_e32 v44, v41
	v_cvt_pk_f16_f32 v33, v42, v43
	s_mov_b32 s12, 0
	v_fma_f32 v42, -v41, v44, 1.0
	v_fmac_f32_e32 v44, v42, v44
	v_div_scale_f32 v42, vcc, s5, v39, s5
	v_mul_f32_e32 v43, v42, v44
	v_fma_f32 v45, -v41, v43, v42
	v_fmac_f32_e32 v43, v45, v44
	v_fma_f32 v41, -v41, v43, v42
	v_div_fmas_f32 v41, v41, v44, v43
	v_div_fixup_f32 v41, v41, v39, s5
	v_mul_f32_e32 v39, 0x3fb8aa3b, v41
	v_fma_f32 v42, v41, s1, -v39
	v_rndne_f32_e32 v43, v39
	v_fmac_f32_e32 v42, 0x32a5705f, v41
	v_sub_f32_e32 v39, v39, v43
	v_add_f32_e32 v39, v39, v42
	v_cvt_i32_f32_e32 v42, v43
	v_mul_f32_e32 v43, 0x3fb8aa3b, v35
	v_fma_f32 v44, v35, s1, -v43
	v_rndne_f32_e32 v45, v43
	v_fmac_f32_e32 v44, 0x32a5705f, v35
	v_sub_f32_e32 v43, v43, v45
	v_add_f32_e32 v43, v43, v44
	v_exp_f32_e32 v39, v39
	v_exp_f32_e32 v43, v43
	v_cvt_i32_f32_e32 v44, v45
	v_cmp_ngt_f32_e32 vcc, s2, v35
	v_ldexp_f32 v57, v39, v42
	v_ldexp_f32 v39, v43, v44
	v_cndmask_b32_e32 v39, 0, v39, vcc
	v_cmp_nlt_f32_e32 vcc, s3, v35
	s_nop 1
	v_cndmask_b32_e32 v35, v107, v39, vcc
	v_add_f32_e32 v39, 1.0, v35
	v_add_f32_e32 v42, -1.0, v39
	v_sub_f32_e32 v43, v42, v39
	v_add_f32_e32 v43, 1.0, v43
	v_sub_f32_e32 v42, v35, v42
	v_add_f32_e32 v44, v42, v43
	v_frexp_mant_f32_e32 v45, v39
	v_cvt_f64_f32_e32 v[42:43], v39
	v_frexp_exp_i32_f64_e32 v42, v[42:43]
	v_cmp_gt_f32_e32 vcc, s10, v45
	s_nop 1
	v_subbrev_co_u32_e32 v50, vcc, 0, v42, vcc
	v_sub_u32_e32 v42, 0, v50
	v_ldexp_f32 v39, v39, v42
	v_ldexp_f32 v42, v44, v42
	v_add_f32_e32 v44, -1.0, v39
	v_add_f32_e32 v43, 1.0, v44
	v_sub_f32_e32 v43, v39, v43
	v_add_f32_e32 v45, v42, v43
	v_add_f32_e32 v43, 1.0, v39
	v_add_f32_e32 v46, -1.0, v43
	v_sub_f32_e32 v39, v39, v46
	v_add_f32_e32 v39, v42, v39
	v_add_f32_e32 v51, v43, v39
	v_rcp_f32_e32 v52, v51
	v_sub_f32_e32 v42, v43, v51
	v_add_f32_e32 v43, v44, v45
	v_add_f32_e32 v39, v39, v42
	v_mul_f32_e32 v54, v43, v52
	v_sub_f32_e32 v42, v44, v43
	v_mul_f32_e32 v44, v51, v54
	v_fma_f32 v46, v54, v51, -v44
	v_fmac_f32_e32 v46, v54, v39
	v_add_f32_e32 v53, v45, v42
	v_add_f32_e32 v42, v44, v46
	v_sub_f32_e32 v45, v43, v42
	v_pk_add_f32 v[48:49], v[42:43], v[44:45] neg_lo:[0,1] neg_hi:[0,1]
	v_mov_b32_e32 v47, v42
	v_pk_add_f32 v[42:43], v[48:49], v[46:47] neg_lo:[0,1] neg_hi:[0,1]
	v_cmp_neq_f32_e32 vcc, s4, v35
	v_add_f32_e32 v43, v53, v43
	v_add_f32_e32 v42, v42, v43
	v_add_f32_e32 v43, v45, v42
	v_mul_f32_e32 v53, v52, v43
	v_mul_f32_e32 v44, v51, v53
	v_fma_f32 v46, v53, v51, -v44
	v_fmac_f32_e32 v46, v53, v39
	v_sub_f32_e32 v39, v45, v43
	v_add_f32_e32 v39, v42, v39
	v_add_f32_e32 v42, v44, v46
	v_sub_f32_e32 v45, v43, v42
	v_pk_add_f32 v[48:49], v[42:43], v[44:45] neg_lo:[0,1] neg_hi:[0,1]
	v_mov_b32_e32 v47, v42
	v_pk_add_f32 v[42:43], v[48:49], v[46:47] neg_lo:[0,1] neg_hi:[0,1]
	s_nop 0
	v_add_f32_e32 v39, v39, v43
	v_add_f32_e32 v39, v42, v39
	v_add_f32_e32 v43, v54, v53
	v_add_f32_e32 v39, v45, v39
	v_sub_f32_e32 v42, v43, v54
	v_mul_f32_e32 v39, v52, v39
	v_sub_f32_e32 v42, v53, v42
	v_add_f32_e32 v44, v42, v39
	v_add_f32_e32 v46, v43, v44
	v_cvt_f32_i32_e32 v42, v50
	v_mul_f32_e32 v47, v46, v46
	v_sub_f32_e32 v43, v46, v43
	v_fmamk_f32 v39, v47, 0x3e9b6dac, v34
	v_sub_f32_e32 v43, v44, v43
	v_fmaak_f32 v39, v47, v39, 0x3f2aaada
	v_ldexp_f32 v48, v43, 1
	v_mul_f32_e32 v43, v46, v47
	v_ldexp_f32 v45, v46, 1
	v_pk_mul_f32 v[46:47], v[42:43], v[38:39]
	s_nop 0
	v_fma_f32 v44, v42, s11, -v46
	v_fmac_f32_e32 v44, 0xb102e308, v42
	v_pk_add_f32 v[42:43], v[46:47], v[44:45]
	s_nop 0
	v_sub_f32_e32 v39, v43, v45
	v_sub_f32_e32 v39, v47, v39
	v_add_f32_e32 v49, v48, v39
	v_mov_b32_e32 v48, v46
	v_pk_add_f32 v[46:47], v[42:43], v[46:47] neg_lo:[0,1] neg_hi:[0,1]
	v_pk_add_f32 v[50:51], v[42:43], v[48:49]
	v_mov_b32_e32 v45, v42
	v_mov_b32_e32 v47, v51
	v_pk_add_f32 v[52:53], v[44:45], v[46:47] neg_lo:[0,1] neg_hi:[0,1]
	v_pk_add_f32 v[44:45], v[44:45], v[46:47]
	v_mov_b32_e32 v48, v49
	v_pk_add_f32 v[46:47], v[44:45], v[42:43] op_sel:[1,0] op_sel_hi:[0,1] neg_lo:[0,1] neg_hi:[0,1]
	v_pk_add_f32 v[54:55], v[50:51], v[46:47] op_sel_hi:[1,0] neg_lo:[0,1] neg_hi:[0,1]
	v_mov_b32_e32 v50, v51
	v_mov_b32_e32 v51, v45
	v_pk_mov_b32 v[46:47], v[42:43], v[46:47] op_sel:[1,0]
	v_mov_b32_e32 v49, v42
	v_pk_add_f32 v[46:47], v[50:51], v[46:47] neg_lo:[0,1] neg_hi:[0,1]
	v_mov_b32_e32 v54, v52
	v_pk_add_f32 v[42:43], v[48:49], v[46:47] neg_lo:[0,1] neg_hi:[0,1]
	v_mov_b32_e32 v53, v45
	v_pk_add_f32 v[46:47], v[54:55], v[42:43]
	s_nop 0
	v_pk_add_f32 v[48:49], v[46:47], v[46:47] op_sel:[0,1] op_sel_hi:[1,0]
	s_nop 0
	v_pk_add_f32 v[44:45], v[44:45], v[48:49] op_sel:[1,0] op_sel_hi:[0,1]
	v_mov_b32_e32 v47, v44
	v_pk_add_f32 v[50:51], v[46:47], v[52:53] neg_lo:[0,1] neg_hi:[0,1]
	v_mov_b32_e32 v43, v48
	v_sub_f32_e32 v39, v46, v50
	v_pk_add_f32 v[42:43], v[42:43], v[50:51] neg_lo:[0,1] neg_hi:[0,1]
	v_sub_f32_e32 v39, v52, v39
	v_add_f32_e32 v39, v42, v39
	v_add_f32_e32 v39, v39, v43
	v_add_f32_e32 v39, v44, v39
	v_cndmask_b32_e32 v39, v107, v39, vcc
	v_cmp_lt_f32_e64 vcc, |v35|, s6
	s_nop 1
	v_cndmask_b32_e32 v35, v39, v35, vcc
	v_add_f32_e32 v35, 0x358637bd, v35
	v_med3_f32 v35, v35, s7, v103
	v_div_scale_f32 v39, s[14:15], v35, v35, s5
	v_rcp_f32_e32 v42, v39
	v_cmp_ngt_f32_e32 vcc, s2, v41
	s_nop 1
	v_cndmask_b32_e32 v43, 0, v57, vcc
	v_cmp_nlt_f32_e32 vcc, s3, v41
	v_fma_f32 v41, -v39, v42, 1.0
	v_fmac_f32_e32 v42, v41, v42
	v_cndmask_b32_e32 v102, v107, v43, vcc
	v_div_scale_f32 v41, vcc, s5, v35, s5
	v_mul_f32_e32 v43, v41, v42
	v_fma_f32 v44, -v39, v43, v41
	v_fmac_f32_e32 v43, v44, v42
	v_fma_f32 v39, -v39, v43, v41
	v_div_fmas_f32 v39, v39, v42, v43
	v_mul_f32_e32 v42, 0x3fb8aa3b, v36
	v_fma_f32 v43, v36, s1, -v42
	v_rndne_f32_e32 v44, v42
	v_fmac_f32_e32 v43, 0x32a5705f, v36
	v_sub_f32_e32 v42, v42, v44
	v_add_f32_e32 v42, v42, v43
	v_div_fixup_f32 v106, v39, v35, s5
	v_exp_f32_e32 v42, v42
	v_cvt_i32_f32_e32 v43, v44
	v_mul_f32_e32 v35, 0x3fb8aa3b, v106
	v_fma_f32 v39, v106, s1, -v35
	v_rndne_f32_e32 v41, v35
	v_fmac_f32_e32 v39, 0x32a5705f, v106
	v_sub_f32_e32 v35, v35, v41
	v_add_f32_e32 v35, v35, v39
	v_ldexp_f32 v39, v42, v43
	v_cmp_ngt_f32_e32 vcc, s2, v36
	v_exp_f32_e32 v35, v35
	v_cvt_i32_f32_e32 v41, v41
	v_cndmask_b32_e32 v39, 0, v39, vcc
	v_cmp_nlt_f32_e32 vcc, s3, v36
	v_ldexp_f32 v35, v35, v41
	s_nop 0
	v_cndmask_b32_e32 v36, v107, v39, vcc
	v_add_f32_e32 v39, 1.0, v36
	v_add_f32_e32 v42, -1.0, v39
	v_sub_f32_e32 v43, v42, v39
	v_add_f32_e32 v43, 1.0, v43
	v_sub_f32_e32 v42, v36, v42
	v_add_f32_e32 v44, v42, v43
	v_frexp_mant_f32_e32 v45, v39
	v_cvt_f64_f32_e32 v[42:43], v39
	v_frexp_exp_i32_f64_e32 v42, v[42:43]
	v_cmp_gt_f32_e32 vcc, s10, v45
	s_nop 1
	v_subbrev_co_u32_e32 v50, vcc, 0, v42, vcc
	v_sub_u32_e32 v42, 0, v50
	v_ldexp_f32 v39, v39, v42
	v_ldexp_f32 v42, v44, v42
	v_add_f32_e32 v44, -1.0, v39
	v_add_f32_e32 v43, 1.0, v44
	v_sub_f32_e32 v43, v39, v43
	v_add_f32_e32 v45, v42, v43
	v_add_f32_e32 v43, 1.0, v39
	v_add_f32_e32 v46, -1.0, v43
	v_sub_f32_e32 v39, v39, v46
	v_add_f32_e32 v39, v42, v39
	v_add_f32_e32 v51, v43, v39
	v_rcp_f32_e32 v52, v51
	v_sub_f32_e32 v42, v43, v51
	v_add_f32_e32 v43, v44, v45
	v_add_f32_e32 v39, v39, v42
	v_mul_f32_e32 v54, v43, v52
	v_sub_f32_e32 v42, v44, v43
	v_mul_f32_e32 v44, v51, v54
	v_fma_f32 v46, v54, v51, -v44
	v_fmac_f32_e32 v46, v54, v39
	v_add_f32_e32 v53, v45, v42
	v_add_f32_e32 v42, v44, v46
	v_sub_f32_e32 v45, v43, v42
	v_pk_add_f32 v[48:49], v[42:43], v[44:45] neg_lo:[0,1] neg_hi:[0,1]
	v_mov_b32_e32 v47, v42
	v_pk_add_f32 v[42:43], v[48:49], v[46:47] neg_lo:[0,1] neg_hi:[0,1]
	v_cmp_neq_f32_e32 vcc, s4, v36
	v_add_f32_e32 v43, v53, v43
	v_add_f32_e32 v42, v42, v43
	v_add_f32_e32 v43, v45, v42
	v_mul_f32_e32 v53, v52, v43
	v_mul_f32_e32 v44, v51, v53
	v_fma_f32 v46, v53, v51, -v44
	v_fmac_f32_e32 v46, v53, v39
	v_sub_f32_e32 v39, v45, v43
	v_add_f32_e32 v39, v42, v39
	v_add_f32_e32 v42, v44, v46
	v_sub_f32_e32 v45, v43, v42
	v_pk_add_f32 v[48:49], v[42:43], v[44:45] neg_lo:[0,1] neg_hi:[0,1]
	v_mov_b32_e32 v47, v42
	v_pk_add_f32 v[42:43], v[48:49], v[46:47] neg_lo:[0,1] neg_hi:[0,1]
	s_nop 0
	v_add_f32_e32 v39, v39, v43
	v_add_f32_e32 v39, v42, v39
	v_add_f32_e32 v43, v54, v53
	v_add_f32_e32 v39, v45, v39
	v_sub_f32_e32 v42, v43, v54
	v_mul_f32_e32 v39, v52, v39
	v_sub_f32_e32 v42, v53, v42
	v_add_f32_e32 v44, v42, v39
	v_add_f32_e32 v46, v43, v44
	v_cvt_f32_i32_e32 v42, v50
	v_mul_f32_e32 v47, v46, v46
	v_sub_f32_e32 v43, v46, v43
	v_fmamk_f32 v39, v47, 0x3e9b6dac, v34
	v_sub_f32_e32 v43, v44, v43
	v_fmaak_f32 v39, v47, v39, 0x3f2aaada
	v_ldexp_f32 v48, v43, 1
	v_mul_f32_e32 v43, v46, v47
	v_ldexp_f32 v45, v46, 1
	v_pk_mul_f32 v[46:47], v[42:43], v[38:39]
	s_nop 0
	v_fma_f32 v44, v42, s11, -v46
	v_fmac_f32_e32 v44, 0xb102e308, v42
	v_pk_add_f32 v[42:43], v[46:47], v[44:45]
	s_nop 0
	v_sub_f32_e32 v39, v43, v45
	v_sub_f32_e32 v39, v47, v39
	v_add_f32_e32 v49, v48, v39
	v_mov_b32_e32 v48, v46
	v_pk_add_f32 v[46:47], v[42:43], v[46:47] neg_lo:[0,1] neg_hi:[0,1]
	v_pk_add_f32 v[50:51], v[42:43], v[48:49]
	v_mov_b32_e32 v45, v42
	v_mov_b32_e32 v47, v51
	v_pk_add_f32 v[52:53], v[44:45], v[46:47] neg_lo:[0,1] neg_hi:[0,1]
	v_pk_add_f32 v[44:45], v[44:45], v[46:47]
	v_mov_b32_e32 v48, v49
	v_pk_add_f32 v[46:47], v[44:45], v[42:43] op_sel:[1,0] op_sel_hi:[0,1] neg_lo:[0,1] neg_hi:[0,1]
	v_pk_add_f32 v[54:55], v[50:51], v[46:47] op_sel_hi:[1,0] neg_lo:[0,1] neg_hi:[0,1]
	v_mov_b32_e32 v50, v51
	v_mov_b32_e32 v51, v45
	v_pk_mov_b32 v[46:47], v[42:43], v[46:47] op_sel:[1,0]
	v_mov_b32_e32 v49, v42
	v_pk_add_f32 v[46:47], v[50:51], v[46:47] neg_lo:[0,1] neg_hi:[0,1]
	v_mov_b32_e32 v54, v52
	v_pk_add_f32 v[42:43], v[48:49], v[46:47] neg_lo:[0,1] neg_hi:[0,1]
	v_mov_b32_e32 v53, v45
	v_pk_add_f32 v[46:47], v[54:55], v[42:43]
	s_nop 0
	v_pk_add_f32 v[48:49], v[46:47], v[46:47] op_sel:[0,1] op_sel_hi:[1,0]
	s_nop 0
	v_pk_add_f32 v[44:45], v[44:45], v[48:49] op_sel:[1,0] op_sel_hi:[0,1]
	v_mov_b32_e32 v47, v44
	v_pk_add_f32 v[50:51], v[46:47], v[52:53] neg_lo:[0,1] neg_hi:[0,1]
	v_mov_b32_e32 v43, v48
	v_sub_f32_e32 v39, v46, v50
	v_pk_add_f32 v[42:43], v[42:43], v[50:51] neg_lo:[0,1] neg_hi:[0,1]
	v_sub_f32_e32 v39, v52, v39
	v_add_f32_e32 v39, v42, v39
	v_add_f32_e32 v39, v39, v43
	v_add_f32_e32 v39, v44, v39
	v_cndmask_b32_e32 v39, v107, v39, vcc
	v_cmp_lt_f32_e64 vcc, |v36|, s6
	s_nop 1
	v_cndmask_b32_e32 v36, v39, v36, vcc
	v_add_f32_e32 v36, 0x358637bd, v36
	v_med3_f32 v36, v36, s7, v103
	v_div_scale_f32 v39, s[14:15], v36, v36, s5
	v_rcp_f32_e32 v42, v39
	v_cmp_ngt_f32_e32 vcc, s2, v106
	s_nop 1
	v_cndmask_b32_e32 v120, 0, v35, vcc
	v_fma_f32 v35, -v39, v42, 1.0
	v_fmac_f32_e32 v42, v35, v42
	v_div_scale_f32 v35, vcc, s5, v36, s5
	v_mul_f32_e32 v41, v35, v42
	v_fma_f32 v43, -v39, v41, v35
	v_fmac_f32_e32 v41, v43, v42
	v_fma_f32 v35, -v39, v41, v35
	v_div_fmas_f32 v35, v35, v42, v41
	v_mul_f32_e32 v41, 0x3fb8aa3b, v37
	v_fma_f32 v42, v37, s1, -v41
	v_rndne_f32_e32 v43, v41
	v_fmac_f32_e32 v42, 0x32a5705f, v37
	v_sub_f32_e32 v41, v41, v43
	v_div_fixup_f32 v121, v35, v36, s5
	v_add_f32_e32 v41, v41, v42
	v_mul_f32_e32 v35, 0x3fb8aa3b, v121
	v_exp_f32_e32 v41, v41
	v_cvt_i32_f32_e32 v42, v43
	v_fma_f32 v36, v121, s1, -v35
	v_rndne_f32_e32 v39, v35
	v_fmac_f32_e32 v36, 0x32a5705f, v121
	v_sub_f32_e32 v35, v35, v39
	v_add_f32_e32 v35, v35, v36
	v_exp_f32_e32 v122, v35
	v_ldexp_f32 v35, v41, v42
	v_cmp_ngt_f32_e32 vcc, s2, v37
	v_cvt_i32_f32_e32 v123, v39
	s_nop 0
	v_cndmask_b32_e32 v35, 0, v35, vcc
	v_cmp_nlt_f32_e32 vcc, s3, v37
	s_nop 1
	v_cndmask_b32_e32 v124, v107, v35, vcc
	v_add_f32_e32 v35, 1.0, v124
	v_add_f32_e32 v36, -1.0, v35
	v_sub_f32_e32 v37, v36, v35
	v_add_f32_e32 v37, 1.0, v37
	v_sub_f32_e32 v36, v124, v36
	v_add_f32_e32 v39, v36, v37
	v_frexp_mant_f32_e32 v41, v35
	v_cvt_f64_f32_e32 v[36:37], v35
	v_frexp_exp_i32_f64_e32 v36, v[36:37]
	v_cmp_gt_f32_e32 vcc, s10, v41
	s_nop 1
	v_subbrev_co_u32_e32 v41, vcc, 0, v36, vcc
	v_sub_u32_e32 v36, 0, v41
	v_ldexp_f32 v35, v35, v36
	v_ldexp_f32 v36, v39, v36
	v_add_f32_e32 v39, -1.0, v35
	v_add_f32_e32 v37, 1.0, v39
	v_sub_f32_e32 v37, v35, v37
	v_add_f32_e32 v42, v36, v37
	v_add_f32_e32 v37, 1.0, v35
	v_add_f32_e32 v43, -1.0, v37
	v_sub_f32_e32 v35, v35, v43
	v_add_f32_e32 v35, v36, v35
	v_add_f32_e32 v48, v37, v35
	v_rcp_f32_e32 v49, v48
	v_sub_f32_e32 v36, v37, v48
	v_add_f32_e32 v37, v39, v42
	v_add_f32_e32 v35, v35, v36
	v_sub_f32_e32 v36, v39, v37
	v_mul_f32_e32 v50, v37, v49
	v_add_f32_e32 v39, v42, v36
	v_mul_f32_e32 v42, v48, v50
	v_fma_f32 v44, v50, v48, -v42
	v_fmac_f32_e32 v44, v50, v35
	v_add_f32_e32 v36, v42, v44
	v_sub_f32_e32 v43, v37, v36
	v_pk_add_f32 v[46:47], v[36:37], v[42:43] neg_lo:[0,1] neg_hi:[0,1]
	v_mov_b32_e32 v45, v36
	v_pk_add_f32 v[36:37], v[46:47], v[44:45] neg_lo:[0,1] neg_hi:[0,1]
	v_cmp_neq_f32_e32 vcc, s4, v124
	v_add_f32_e32 v37, v39, v37
	v_add_f32_e32 v36, v36, v37
	v_add_f32_e32 v37, v43, v36
	v_mul_f32_e32 v39, v49, v37
	v_mul_f32_e32 v42, v48, v39
	v_fma_f32 v44, v39, v48, -v42
	v_fmac_f32_e32 v44, v39, v35
	v_sub_f32_e32 v35, v43, v37
	v_add_f32_e32 v35, v36, v35
	v_add_f32_e32 v36, v42, v44
	v_sub_f32_e32 v43, v37, v36
	v_pk_add_f32 v[46:47], v[36:37], v[42:43] neg_lo:[0,1] neg_hi:[0,1]
	v_mov_b32_e32 v45, v36
	v_pk_add_f32 v[36:37], v[46:47], v[44:45] neg_lo:[0,1] neg_hi:[0,1]
	s_nop 0
	v_add_f32_e32 v35, v35, v37
	v_add_f32_e32 v35, v36, v35
	v_add_f32_e32 v36, v50, v39
	v_add_f32_e32 v35, v43, v35
	v_sub_f32_e32 v37, v36, v50
	v_mul_f32_e32 v35, v49, v35
	v_sub_f32_e32 v37, v39, v37
	v_add_f32_e32 v35, v37, v35
	v_add_f32_e32 v39, v36, v35
	v_mul_f32_e32 v42, v39, v39
	v_fmac_f32_e32 v34, 0x3e9b6dac, v42
	v_fmac_f32_e32 v56, v42, v34
	v_cvt_f32_i32_e32 v34, v41
	v_sub_f32_e32 v36, v39, v36
	v_sub_f32_e32 v35, v35, v36
	v_ldexp_f32 v37, v39, 1
	v_ldexp_f32 v41, v35, 1
	v_mul_f32_e32 v35, v39, v42
	v_mov_b32_e32 v39, v56
	v_pk_mul_f32 v[38:39], v[34:35], v[38:39]
	s_nop 0
	v_fma_f32 v36, v34, s11, -v38
	v_fmac_f32_e32 v36, 0xb102e308, v34
	v_pk_add_f32 v[104:105], v[38:39], v[36:37]
	s_nop 0
	v_sub_f32_e32 v34, v105, v37
	v_sub_f32_e32 v34, v39, v34
	v_add_f32_e32 v35, v41, v34
	v_mov_b32_e32 v34, v38
	v_pk_add_f32 v[38:39], v[104:105], v[38:39] neg_lo:[0,1] neg_hi:[0,1]
	v_pk_add_f32 v[42:43], v[104:105], v[34:35]
	v_mov_b32_e32 v37, v104
	v_mov_b32_e32 v39, v43
	v_pk_add_f32 v[110:111], v[36:37], v[38:39]
	v_pk_add_f32 v[108:109], v[36:37], v[38:39] neg_lo:[0,1] neg_hi:[0,1]
	v_pk_add_f32 v[36:37], v[110:111], v[104:105] op_sel:[1,0] op_sel_hi:[0,1] neg_lo:[0,1] neg_hi:[0,1]
	v_pk_add_f32 v[112:113], v[42:43], v[36:37] op_sel_hi:[1,0] neg_lo:[0,1] neg_hi:[0,1]
	v_mov_b32_e32 v38, v43
	v_mov_b32_e32 v39, v111
	v_pk_mov_b32 v[36:37], v[104:105], v[36:37] op_sel:[1,0]
	v_mov_b32_e32 v116, v35
	v_lshl_add_u64 v[34:35], s[52:53], 0, v[62:63]
	v_pk_add_f32 v[114:115], v[38:39], v[36:37] neg_lo:[0,1] neg_hi:[0,1]
	v_lshl_add_u64 v[34:35], v[34:35], 0, v[118:119]
	v_lshlrev_b32_e32 v36, 4, v1
	v_mov_b32_e32 v37, v63
	v_lshl_add_u64 v[34:35], v[34:35], 0, v[36:37]
	global_load_dwordx4 v[98:101], v[34:35], off
	global_load_dwordx4 v[70:73], v[34:35], off offset:256
	global_load_dwordx4 v[78:81], v[34:35], off offset:512
	global_load_dwordx4 v[86:89], v[34:35], off offset:768
	global_load_dwordx4 v[94:97], v[34:35], off offset:1024
	global_load_dwordx4 v[90:93], v[34:35], off offset:1280
	global_load_dwordx4 v[82:85], v[34:35], off offset:1536
	global_load_dwordx4 v[74:77], v[34:35], off offset:1792
	global_load_dwordx4 v[66:69], v[34:35], off offset:2048
	global_load_dwordx4 v[58:61], v[34:35], off offset:2304
	global_load_dwordx4 v[54:57], v[34:35], off offset:2560
	global_load_dwordx4 v[50:53], v[34:35], off offset:2816
	global_load_dwordx4 v[46:49], v[34:35], off offset:3072
	global_load_dwordx4 v[42:45], v[34:35], off offset:3328
	global_load_dwordx4 v[38:41], v[34:35], off offset:3584
	s_nop 0
	global_load_dwordx4 v[34:37], v[34:35], off offset:3840
	v_mov_b32_e32 v117, v104
	v_pk_add_f32 v[104:105], v[116:117], v[114:115] neg_lo:[0,1] neg_hi:[0,1]
	v_mov_b32_e32 v112, v108
	v_pk_add_f32 v[112:113], v[112:113], v[104:105]
	v_mov_b32_e32 v109, v111
	v_pk_add_f32 v[114:115], v[112:113], v[112:113] op_sel:[0,1] op_sel_hi:[1,0]
	v_lshlrev_b32_e32 v1, 5, v1
	v_pk_add_f32 v[110:111], v[110:111], v[114:115] op_sel:[1,0] op_sel_hi:[0,1]
	v_mov_b32_e32 v113, v110
	v_pk_add_f32 v[116:117], v[112:113], v[108:109] neg_lo:[0,1] neg_hi:[0,1]
	v_mov_b32_e32 v105, v114
	v_sub_f32_e32 v109, v112, v116
	v_pk_add_f32 v[104:105], v[104:105], v[116:117] neg_lo:[0,1] neg_hi:[0,1]
	v_sub_f32_e32 v108, v108, v109
	v_add_f32_e32 v104, v104, v108
	v_add_f32_e32 v104, v104, v105
	v_add_f32_e32 v104, v110, v104
	v_cndmask_b32_e32 v104, v107, v104, vcc
	v_cmp_lt_f32_e64 vcc, |v124|, s6
	v_lshlrev_b32_e32 v114, 3, v64
	v_or3_b32 v62, v118, v0, v62
	v_cndmask_b32_e32 v104, v104, v124, vcc
	v_add_f32_e32 v104, 0x358637bd, v104
	v_med3_f32 v108, v104, s7, v103
	v_div_scale_f32 v109, s[6:7], v108, v108, s5
	v_rcp_f32_e32 v110, v109
	v_cmp_nlt_f32_e32 vcc, s3, v106
	v_ldexp_f32 v106, v122, v123
	v_or3_b32 v122, v65, v1, v114
	v_fma_f32 v111, -v109, v110, 1.0
	v_cndmask_b32_e32 v103, v107, v120, vcc
	v_fmac_f32_e32 v110, v111, v110
	v_div_scale_f32 v111, vcc, s5, v108, s5
	v_mul_f32_e32 v112, v111, v110
	v_fma_f32 v113, -v109, v112, v111
	v_fmac_f32_e32 v112, v113, v110
	v_fma_f32 v109, -v109, v112, v111
	v_div_fmas_f32 v109, v109, v110, v112
	v_div_fixup_f32 v108, v109, v108, s5
	v_mul_f32_e32 v109, 0x3fb8aa3b, v108
	v_fma_f32 v110, v108, s1, -v109
	v_rndne_f32_e32 v111, v109
	v_fmac_f32_e32 v110, 0x32a5705f, v108
	v_sub_f32_e32 v109, v109, v111
	v_add_f32_e32 v109, v109, v110
	v_exp_f32_e32 v109, v109
	v_cvt_i32_f32_e32 v110, v111
	v_cmp_ngt_f32_e32 vcc, s2, v121
	v_pk_add_f32 v[104:105], v[102:103], 1.0 op_sel_hi:[1,0] neg_lo:[1,0] neg_hi:[1,0]
	v_lshl_add_u64 v[0:1], s[52:53], 0, v[62:63]
	v_cndmask_b32_e32 v106, 0, v106, vcc
	v_cmp_nlt_f32_e32 vcc, s3, v121
	v_ldexp_f32 v109, v109, v110
	s_mov_b64 s[6:7], 0x1800
	v_cndmask_b32_e32 v106, v107, v106, vcc
	v_cmp_ngt_f32_e32 vcc, s2, v108
	v_pk_mul_f32 v[110:111], v[104:105], -2.0 op_sel_hi:[1,0]
	v_cmp_eq_u32_e64 s[0:1], 0, v64
	v_cndmask_b32_e32 v109, 0, v109, vcc
	v_cmp_nlt_f32_e32 vcc, s3, v108
	v_cmp_gt_u32_e64 s[2:3], 2, v64
	v_cmp_eq_u32_e64 s[4:5], 3, v64
	v_cndmask_b32_e32 v107, v107, v109, vcc
	v_pk_add_f32 v[108:109], v[106:107], 1.0 op_sel_hi:[1,0] neg_lo:[1,0] neg_hi:[1,0]
	v_lshl_add_u64 v[0:1], v[0:1], 0, s[6:7]
	v_pk_mul_f32 v[112:113], v[108:109], -2.0 op_sel_hi:[1,0]
	s_mov_b64 s[6:7], 0x1000
	v_mov_b32_e32 v165, v3
	v_mov_b32_e32 v166, v4
	v_mov_b32_e32 v167, v5
	v_mov_b32_e32 v168, v6
	v_mov_b32_e32 v169, v7
	v_mov_b32_e32 v170, v8
	v_mov_b32_e32 v3, v166
	v_mov_b32_e32 v4, v168
	v_mov_b32_e32 v5, v170
	v_mov_b32_e32 v6, v165
	v_mov_b32_e32 v7, v167
	v_mov_b32_e32 v8, v169
	v_mov_b32_e32 v165, v11
	v_mov_b32_e32 v166, v12
	v_mov_b32_e32 v167, v13
	v_mov_b32_e32 v168, v14
	v_mov_b32_e32 v169, v15
	v_mov_b32_e32 v170, v16
	v_mov_b32_e32 v11, v166
	v_mov_b32_e32 v12, v168
	v_mov_b32_e32 v13, v170
	v_mov_b32_e32 v14, v165
	v_mov_b32_e32 v15, v167
	v_mov_b32_e32 v16, v169
	v_mov_b32_e32 v165, v19
	v_mov_b32_e32 v166, v20
	v_mov_b32_e32 v167, v21
	v_mov_b32_e32 v168, v22
	v_mov_b32_e32 v169, v23
	v_mov_b32_e32 v170, v24
	v_mov_b32_e32 v19, v166
	v_mov_b32_e32 v20, v168
	v_mov_b32_e32 v21, v170
	v_mov_b32_e32 v22, v165
	v_mov_b32_e32 v23, v167
	v_mov_b32_e32 v24, v169
	v_mov_b32_e32 v165, v27
	v_mov_b32_e32 v166, v28
	v_mov_b32_e32 v167, v29
	v_mov_b32_e32 v168, v30
	v_mov_b32_e32 v169, v31
	v_mov_b32_e32 v170, v32
	v_mov_b32_e32 v27, v166
	v_mov_b32_e32 v28, v168
	v_mov_b32_e32 v29, v170
	v_mov_b32_e32 v30, v165
	v_mov_b32_e32 v31, v167
	v_mov_b32_e32 v32, v169
	v_mov_b32_e32 v124, 0
	v_mov_b32_e32 v125, 0
	v_mov_b32_e32 v126, 0
	v_mov_b32_e32 v127, 0
	v_mov_b32_e32 v128, 0
	v_mov_b32_e32 v129, 0
	v_mov_b32_e32 v130, 0
	v_mov_b32_e32 v131, 0
	v_mov_b32_e32 v148, 0
	v_mov_b32_e32 v149, 0
	v_mov_b32_e32 v150, 0
	v_mov_b32_e32 v151, 0
	v_mov_b32_e32 v152, v104
	v_mov_b32_e32 v153, v105
	v_mov_b32_e32 v154, v108
	v_mov_b32_e32 v155, v109
	s_branch .LBB3_169

.LBB3_169:
	s_cmp_lt_u32 s12, 64
	s_cbranch_scc1 .Lmy_l1_main
	s_cmp_lg_u32 s12, 64
	s_cbranch_scc1 .LBB3_168
	v_mov_b32_e32 v164, v122
	s_waitcnt vmcnt(15)
	v_mfma_f32_16x16x32_f16 v[132:135], v[2:5], v[124:127], v[98:101]
	v_mfma_f32_16x16x32_f16 v[136:139], v[10:13], v[124:127], v[98:101]
	v_mfma_f32_16x16x32_f16 v[140:143], v[18:21], v[124:127], v[98:101]
	v_mfma_f32_16x16x32_f16 v[144:147], v[26:29], v[124:127], v[98:101]
	v_mfma_f32_16x16x32_f16 v[132:135], v[6:9], v[128:131], v[132:135]
	s_nop 2
	v_mfma_f32_16x16x32_f16 v[136:139], v[14:17], v[128:131], v[136:139]
	s_nop 2
	v_mfma_f32_16x16x32_f16 v[140:143], v[22:25], v[128:131], v[140:143]
	s_nop 2
	v_mfma_f32_16x16x32_f16 v[144:147], v[30:33], v[128:131], v[144:147]
	v_cndmask_b32_e64 v160, v136, v132, s[0:1]
	v_cndmask_b32_e64 v161, v137, v133, s[0:1]
	v_cndmask_b32_e64 v162, v138, v134, s[0:1]
	v_cndmask_b32_e64 v163, v139, v135, s[0:1]
	v_cndmask_b32_e64 v160, v140, v160, s[2:3]
	v_cndmask_b32_e64 v161, v141, v161, s[2:3]
	v_cndmask_b32_e64 v162, v142, v162, s[2:3]
	v_cndmask_b32_e64 v163, v143, v163, s[2:3]
	v_cndmask_b32_e64 v156, v160, v144, s[4:5]
	v_cndmask_b32_e64 v157, v161, v145, s[4:5]
	v_exp_f32_e32 v156, v156
	v_exp_f32_e32 v157, v157
	v_cndmask_b32_e64 v158, v162, v146, s[4:5]
	v_cndmask_b32_e64 v159, v163, v147, s[4:5]
	v_pk_add_f32 v[156:157], v[156:157], 1.0 op_sel_hi:[1,0]
	v_exp_f32_e32 v158, v158
	v_rcp_f32_e32 v156, v156
	v_rcp_f32_e32 v157, v157
	v_exp_f32_e32 v159, v159
	v_pk_fma_f32 v[148:149], v[110:111], v[156:157], v[152:153]
	v_pk_add_f32 v[158:159], v[158:159], 1.0 op_sel_hi:[1,0]
	v_cvt_pk_f16_f32 v124, v148, v149
	v_rcp_f32_e32 v158, v158
	v_rcp_f32_e32 v159, v159
	v_mov_b32_dpp v125, v124 quad_perm:[1,2,3,0] row_mask:0xf bank_mask:0xf bound_ctrl:1
	v_mov_b32_dpp v126, v124 quad_perm:[2,3,0,1] row_mask:0xf bank_mask:0xf bound_ctrl:1
	v_mov_b32_dpp v127, v124 quad_perm:[3,0,1,2] row_mask:0xf bank_mask:0xf bound_ctrl:1
	v_pk_fma_f32 v[150:151], v[112:113], v[158:159], v[154:155]
	s_nop 0
	v_cvt_pk_f16_f32 v128, v150, v151
	ds_write_b32 v164, v124 offset:0
	v_fma_f32 v152, v102, v148, v104
	v_mov_b32_dpp v129, v128 quad_perm:[1,2,3,0] row_mask:0xf bank_mask:0xf bound_ctrl:1
	v_mov_b32_dpp v130, v128 quad_perm:[2,3,0,1] row_mask:0xf bank_mask:0xf bound_ctrl:1
	v_mov_b32_dpp v131, v128 quad_perm:[3,0,1,2] row_mask:0xf bank_mask:0xf bound_ctrl:1
	ds_write_b32 v164, v128 offset:4
	v_fma_f32 v153, v103, v149, v105
	v_fma_f32 v154, v106, v150, v108
	v_fma_f32 v155, v107, v151, v109
	s_branch .LBB3_168
.Lmy_l1_main:
	s_bitcmp1_b32 s12, 0
	s_cselect_b32 s10, 0x2100, 0
	s_nop 0
	v_add_u32_e32 v164, s10, v122
	s_waitcnt vmcnt(15)
	v_mfma_f32_16x16x32_f16 v[132:135], v[2:5], v[124:127], v[98:101]
	v_mfma_f32_16x16x32_f16 v[136:139], v[10:13], v[124:127], v[98:101]
	v_mfma_f32_16x16x32_f16 v[140:143], v[18:21], v[124:127], v[98:101]
	v_mfma_f32_16x16x32_f16 v[144:147], v[26:29], v[124:127], v[98:101]
	global_load_dwordx4 v[98:101], v[0:1], off offset:-2048
	v_mfma_f32_16x16x32_f16 v[132:135], v[6:9], v[128:131], v[132:135]
	s_nop 2
	v_mfma_f32_16x16x32_f16 v[136:139], v[14:17], v[128:131], v[136:139]
	s_nop 2
	v_mfma_f32_16x16x32_f16 v[140:143], v[22:25], v[128:131], v[140:143]
	s_nop 2
	v_mfma_f32_16x16x32_f16 v[144:147], v[30:33], v[128:131], v[144:147]
	v_cndmask_b32_e64 v160, v136, v132, s[0:1]
	v_cndmask_b32_e64 v161, v137, v133, s[0:1]
	v_cndmask_b32_e64 v162, v138, v134, s[0:1]
	v_cndmask_b32_e64 v163, v139, v135, s[0:1]
	v_cndmask_b32_e64 v160, v140, v160, s[2:3]
	v_cndmask_b32_e64 v161, v141, v161, s[2:3]
	v_cndmask_b32_e64 v162, v142, v162, s[2:3]
	v_cndmask_b32_e64 v163, v143, v163, s[2:3]
	v_cndmask_b32_e64 v156, v160, v144, s[4:5]
	v_cndmask_b32_e64 v157, v161, v145, s[4:5]
	v_exp_f32_e32 v156, v156
	v_exp_f32_e32 v157, v157
	v_cndmask_b32_e64 v158, v162, v146, s[4:5]
	v_cndmask_b32_e64 v159, v163, v147, s[4:5]
	v_pk_add_f32 v[156:157], v[156:157], 1.0 op_sel_hi:[1,0]
	v_exp_f32_e32 v158, v158
	v_rcp_f32_e32 v156, v156
	v_rcp_f32_e32 v157, v157
	v_exp_f32_e32 v159, v159
	v_pk_fma_f32 v[148:149], v[110:111], v[156:157], v[152:153]
	v_pk_add_f32 v[158:159], v[158:159], 1.0 op_sel_hi:[1,0]
	v_cvt_pk_f16_f32 v124, v148, v149
	v_rcp_f32_e32 v158, v158
	v_rcp_f32_e32 v159, v159
	v_mov_b32_dpp v125, v124 quad_perm:[1,2,3,0] row_mask:0xf bank_mask:0xf bound_ctrl:1
	v_mov_b32_dpp v126, v124 quad_perm:[2,3,0,1] row_mask:0xf bank_mask:0xf bound_ctrl:1
	v_mov_b32_dpp v127, v124 quad_perm:[3,0,1,2] row_mask:0xf bank_mask:0xf bound_ctrl:1
	v_pk_fma_f32 v[150:151], v[112:113], v[158:159], v[154:155]
	s_waitcnt vmcnt(15)
	v_mfma_f32_16x16x32_f16 v[132:135], v[2:5], v[124:127], v[70:73]
	v_cvt_pk_f16_f32 v128, v150, v151
	s_nop 0
	v_mfma_f32_16x16x32_f16 v[136:139], v[10:13], v[124:127], v[70:73]
	v_mov_b32_dpp v129, v128 quad_perm:[1,2,3,0] row_mask:0xf bank_mask:0xf bound_ctrl:1
	v_mov_b32_dpp v130, v128 quad_perm:[2,3,0,1] row_mask:0xf bank_mask:0xf bound_ctrl:1
	v_mfma_f32_16x16x32_f16 v[140:143], v[18:21], v[124:127], v[70:73]
	v_mov_b32_dpp v131, v128 quad_perm:[3,0,1,2] row_mask:0xf bank_mask:0xf bound_ctrl:1
	s_nop 0
	v_mfma_f32_16x16x32_f16 v[144:147], v[26:29], v[124:127], v[70:73]
	v_mfma_f32_16x16x32_f16 v[132:135], v[6:9], v[128:131], v[132:135]
	v_fma_f32 v154, v106, v150, v108
	v_fma_f32 v155, v107, v151, v109
	ds_write_b32 v164, v124 offset:0
	v_mfma_f32_16x16x32_f16 v[136:139], v[14:17], v[128:131], v[136:139]
	v_fma_f32 v152, v102, v148, v104
	v_fma_f32 v153, v103, v149, v105
	ds_write_b32 v164, v128 offset:4
	v_mfma_f32_16x16x32_f16 v[140:143], v[22:25], v[128:131], v[140:143]
	global_load_dwordx4 v[70:73], v[0:1], off offset:-1792
	s_nop 1
	v_mfma_f32_16x16x32_f16 v[144:147], v[30:33], v[128:131], v[144:147]
	v_cndmask_b32_e64 v160, v136, v132, s[0:1]
	v_cndmask_b32_e64 v161, v137, v133, s[0:1]
	v_cndmask_b32_e64 v162, v138, v134, s[0:1]
	v_cndmask_b32_e64 v163, v139, v135, s[0:1]
	v_cndmask_b32_e64 v160, v140, v160, s[2:3]
	v_cndmask_b32_e64 v161, v141, v161, s[2:3]
	v_cndmask_b32_e64 v162, v142, v162, s[2:3]
	v_cndmask_b32_e64 v163, v143, v163, s[2:3]
	v_cndmask_b32_e64 v156, v160, v144, s[4:5]
	v_cndmask_b32_e64 v157, v161, v145, s[4:5]
	v_exp_f32_e32 v156, v156
	v_exp_f32_e32 v157, v157
	v_cndmask_b32_e64 v158, v162, v146, s[4:5]
	v_cndmask_b32_e64 v159, v163, v147, s[4:5]
	v_pk_add_f32 v[156:157], v[156:157], 1.0 op_sel_hi:[1,0]
	v_exp_f32_e32 v158, v158
	v_rcp_f32_e32 v156, v156
	v_rcp_f32_e32 v157, v157
	v_exp_f32_e32 v159, v159
	v_pk_fma_f32 v[148:149], v[110:111], v[156:157], v[152:153]
	v_pk_add_f32 v[158:159], v[158:159], 1.0 op_sel_hi:[1,0]
	v_cvt_pk_f16_f32 v124, v148, v149
	v_rcp_f32_e32 v158, v158
	v_rcp_f32_e32 v159, v159
	v_mov_b32_dpp v125, v124 quad_perm:[1,2,3,0] row_mask:0xf bank_mask:0xf bound_ctrl:1
	v_mov_b32_dpp v126, v124 quad_perm:[2,3,0,1] row_mask:0xf bank_mask:0xf bound_ctrl:1
	v_mov_b32_dpp v127, v124 quad_perm:[3,0,1,2] row_mask:0xf bank_mask:0xf bound_ctrl:1
	v_pk_fma_f32 v[150:151], v[112:113], v[158:159], v[154:155]
	s_waitcnt vmcnt(15)
	v_mfma_f32_16x16x32_f16 v[132:135], v[2:5], v[124:127], v[78:81]
	v_cvt_pk_f16_f32 v128, v150, v151
	s_nop 0
	v_mfma_f32_16x16x32_f16 v[136:139], v[10:13], v[124:127], v[78:81]
	v_mov_b32_dpp v129, v128 quad_perm:[1,2,3,0] row_mask:0xf bank_mask:0xf bound_ctrl:1
	v_mov_b32_dpp v130, v128 quad_perm:[2,3,0,1] row_mask:0xf bank_mask:0xf bound_ctrl:1
	v_mfma_f32_16x16x32_f16 v[140:143], v[18:21], v[124:127], v[78:81]
	v_mov_b32_dpp v131, v128 quad_perm:[3,0,1,2] row_mask:0xf bank_mask:0xf bound_ctrl:1
	s_nop 0
	v_mfma_f32_16x16x32_f16 v[144:147], v[26:29], v[124:127], v[78:81]
	v_mfma_f32_16x16x32_f16 v[132:135], v[6:9], v[128:131], v[132:135]
	v_fma_f32 v154, v106, v150, v108
	v_fma_f32 v155, v107, v151, v109
	ds_write_b32 v164, v124 offset:528
	v_mfma_f32_16x16x32_f16 v[136:139], v[14:17], v[128:131], v[136:139]
	v_fma_f32 v152, v102, v148, v104
	v_fma_f32 v153, v103, v149, v105
	ds_write_b32 v164, v128 offset:532
	v_mfma_f32_16x16x32_f16 v[140:143], v[22:25], v[128:131], v[140:143]
	global_load_dwordx4 v[78:81], v[0:1], off offset:-1536
	s_nop 1
	v_mfma_f32_16x16x32_f16 v[144:147], v[30:33], v[128:131], v[144:147]
	v_cndmask_b32_e64 v160, v136, v132, s[0:1]
	v_cndmask_b32_e64 v161, v137, v133, s[0:1]
	v_cndmask_b32_e64 v162, v138, v134, s[0:1]
	v_cndmask_b32_e64 v163, v139, v135, s[0:1]
	v_cndmask_b32_e64 v160, v140, v160, s[2:3]
	v_cndmask_b32_e64 v161, v141, v161, s[2:3]
	v_cndmask_b32_e64 v162, v142, v162, s[2:3]
	v_cndmask_b32_e64 v163, v143, v163, s[2:3]
	v_cndmask_b32_e64 v156, v160, v144, s[4:5]
	v_cndmask_b32_e64 v157, v161, v145, s[4:5]
	v_exp_f32_e32 v156, v156
	v_exp_f32_e32 v157, v157
	v_cndmask_b32_e64 v158, v162, v146, s[4:5]
	v_cndmask_b32_e64 v159, v163, v147, s[4:5]
	v_pk_add_f32 v[156:157], v[156:157], 1.0 op_sel_hi:[1,0]
	v_exp_f32_e32 v158, v158
	v_rcp_f32_e32 v156, v156
	v_rcp_f32_e32 v157, v157
	v_exp_f32_e32 v159, v159
	v_pk_fma_f32 v[148:149], v[110:111], v[156:157], v[152:153]
	v_pk_add_f32 v[158:159], v[158:159], 1.0 op_sel_hi:[1,0]
	v_cvt_pk_f16_f32 v124, v148, v149
	v_rcp_f32_e32 v158, v158
	v_rcp_f32_e32 v159, v159
	v_mov_b32_dpp v125, v124 quad_perm:[1,2,3,0] row_mask:0xf bank_mask:0xf bound_ctrl:1
	v_mov_b32_dpp v126, v124 quad_perm:[2,3,0,1] row_mask:0xf bank_mask:0xf bound_ctrl:1
	v_mov_b32_dpp v127, v124 quad_perm:[3,0,1,2] row_mask:0xf bank_mask:0xf bound_ctrl:1
	v_pk_fma_f32 v[150:151], v[112:113], v[158:159], v[154:155]
	s_waitcnt vmcnt(15)
	v_mfma_f32_16x16x32_f16 v[132:135], v[2:5], v[124:127], v[86:89]
	v_cvt_pk_f16_f32 v128, v150, v151
	s_nop 0
	v_mfma_f32_16x16x32_f16 v[136:139], v[10:13], v[124:127], v[86:89]
	v_mov_b32_dpp v129, v128 quad_perm:[1,2,3,0] row_mask:0xf bank_mask:0xf bound_ctrl:1
	v_mov_b32_dpp v130, v128 quad_perm:[2,3,0,1] row_mask:0xf bank_mask:0xf bound_ctrl:1
	v_mfma_f32_16x16x32_f16 v[140:143], v[18:21], v[124:127], v[86:89]
	v_mov_b32_dpp v131, v128 quad_perm:[3,0,1,2] row_mask:0xf bank_mask:0xf bound_ctrl:1
	s_nop 0
	v_mfma_f32_16x16x32_f16 v[144:147], v[26:29], v[124:127], v[86:89]
	v_mfma_f32_16x16x32_f16 v[132:135], v[6:9], v[128:131], v[132:135]
	v_fma_f32 v154, v106, v150, v108
	v_fma_f32 v155, v107, v151, v109
	ds_write_b32 v164, v124 offset:1056
	v_mfma_f32_16x16x32_f16 v[136:139], v[14:17], v[128:131], v[136:139]
	v_fma_f32 v152, v102, v148, v104
	v_fma_f32 v153, v103, v149, v105
	ds_write_b32 v164, v128 offset:1060
	v_mfma_f32_16x16x32_f16 v[140:143], v[22:25], v[128:131], v[140:143]
	global_load_dwordx4 v[86:89], v[0:1], off offset:-1280
	s_nop 1
	v_mfma_f32_16x16x32_f16 v[144:147], v[30:33], v[128:131], v[144:147]
	v_cndmask_b32_e64 v160, v136, v132, s[0:1]
	v_cndmask_b32_e64 v161, v137, v133, s[0:1]
	v_cndmask_b32_e64 v162, v138, v134, s[0:1]
	v_cndmask_b32_e64 v163, v139, v135, s[0:1]
	v_cndmask_b32_e64 v160, v140, v160, s[2:3]
	v_cndmask_b32_e64 v161, v141, v161, s[2:3]
	v_cndmask_b32_e64 v162, v142, v162, s[2:3]
	v_cndmask_b32_e64 v163, v143, v163, s[2:3]
	v_cndmask_b32_e64 v156, v160, v144, s[4:5]
	v_cndmask_b32_e64 v157, v161, v145, s[4:5]
	v_exp_f32_e32 v156, v156
	v_exp_f32_e32 v157, v157
	v_cndmask_b32_e64 v158, v162, v146, s[4:5]
	v_cndmask_b32_e64 v159, v163, v147, s[4:5]
	v_pk_add_f32 v[156:157], v[156:157], 1.0 op_sel_hi:[1,0]
	v_exp_f32_e32 v158, v158
	v_rcp_f32_e32 v156, v156
	v_rcp_f32_e32 v157, v157
	v_exp_f32_e32 v159, v159
	v_pk_fma_f32 v[148:149], v[110:111], v[156:157], v[152:153]
	v_pk_add_f32 v[158:159], v[158:159], 1.0 op_sel_hi:[1,0]
	v_cvt_pk_f16_f32 v124, v148, v149
	v_rcp_f32_e32 v158, v158
	v_rcp_f32_e32 v159, v159
	v_mov_b32_dpp v125, v124 quad_perm:[1,2,3,0] row_mask:0xf bank_mask:0xf bound_ctrl:1
	v_mov_b32_dpp v126, v124 quad_perm:[2,3,0,1] row_mask:0xf bank_mask:0xf bound_ctrl:1
	v_mov_b32_dpp v127, v124 quad_perm:[3,0,1,2] row_mask:0xf bank_mask:0xf bound_ctrl:1
	v_pk_fma_f32 v[150:151], v[112:113], v[158:159], v[154:155]
	s_waitcnt vmcnt(15)
	v_mfma_f32_16x16x32_f16 v[132:135], v[2:5], v[124:127], v[94:97]
	v_cvt_pk_f16_f32 v128, v150, v151
	s_nop 0
	v_mfma_f32_16x16x32_f16 v[136:139], v[10:13], v[124:127], v[94:97]
	v_mov_b32_dpp v129, v128 quad_perm:[1,2,3,0] row_mask:0xf bank_mask:0xf bound_ctrl:1
	v_mov_b32_dpp v130, v128 quad_perm:[2,3,0,1] row_mask:0xf bank_mask:0xf bound_ctrl:1
	v_mfma_f32_16x16x32_f16 v[140:143], v[18:21], v[124:127], v[94:97]
	v_mov_b32_dpp v131, v128 quad_perm:[3,0,1,2] row_mask:0xf bank_mask:0xf bound_ctrl:1
	s_nop 0
	v_mfma_f32_16x16x32_f16 v[144:147], v[26:29], v[124:127], v[94:97]
	v_mfma_f32_16x16x32_f16 v[132:135], v[6:9], v[128:131], v[132:135]
	v_fma_f32 v154, v106, v150, v108
	v_fma_f32 v155, v107, v151, v109
	ds_write_b32 v164, v124 offset:1584
	v_mfma_f32_16x16x32_f16 v[136:139], v[14:17], v[128:131], v[136:139]
	v_fma_f32 v152, v102, v148, v104
	v_fma_f32 v153, v103, v149, v105
	ds_write_b32 v164, v128 offset:1588
	v_mfma_f32_16x16x32_f16 v[140:143], v[22:25], v[128:131], v[140:143]
	global_load_dwordx4 v[94:97], v[0:1], off offset:-1024
	s_nop 1
	v_mfma_f32_16x16x32_f16 v[144:147], v[30:33], v[128:131], v[144:147]
	v_cndmask_b32_e64 v160, v136, v132, s[0:1]
	v_cndmask_b32_e64 v161, v137, v133, s[0:1]
	v_cndmask_b32_e64 v162, v138, v134, s[0:1]
	v_cndmask_b32_e64 v163, v139, v135, s[0:1]
	v_cndmask_b32_e64 v160, v140, v160, s[2:3]
	v_cndmask_b32_e64 v161, v141, v161, s[2:3]
	v_cndmask_b32_e64 v162, v142, v162, s[2:3]
	v_cndmask_b32_e64 v163, v143, v163, s[2:3]
	v_cndmask_b32_e64 v156, v160, v144, s[4:5]
	v_cndmask_b32_e64 v157, v161, v145, s[4:5]
	v_exp_f32_e32 v156, v156
	v_exp_f32_e32 v157, v157
	v_cndmask_b32_e64 v158, v162, v146, s[4:5]
	v_cndmask_b32_e64 v159, v163, v147, s[4:5]
	v_pk_add_f32 v[156:157], v[156:157], 1.0 op_sel_hi:[1,0]
	v_exp_f32_e32 v158, v158
	v_rcp_f32_e32 v156, v156
	v_rcp_f32_e32 v157, v157
	v_exp_f32_e32 v159, v159
	v_pk_fma_f32 v[148:149], v[110:111], v[156:157], v[152:153]
	v_pk_add_f32 v[158:159], v[158:159], 1.0 op_sel_hi:[1,0]
	v_cvt_pk_f16_f32 v124, v148, v149
	v_rcp_f32_e32 v158, v158
	v_rcp_f32_e32 v159, v159
	v_mov_b32_dpp v125, v124 quad_perm:[1,2,3,0] row_mask:0xf bank_mask:0xf bound_ctrl:1
	v_mov_b32_dpp v126, v124 quad_perm:[2,3,0,1] row_mask:0xf bank_mask:0xf bound_ctrl:1
	v_mov_b32_dpp v127, v124 quad_perm:[3,0,1,2] row_mask:0xf bank_mask:0xf bound_ctrl:1
	v_pk_fma_f32 v[150:151], v[112:113], v[158:159], v[154:155]
	s_waitcnt vmcnt(15)
	v_mfma_f32_16x16x32_f16 v[132:135], v[2:5], v[124:127], v[90:93]
	v_cvt_pk_f16_f32 v128, v150, v151
	s_nop 0
	v_mfma_f32_16x16x32_f16 v[136:139], v[10:13], v[124:127], v[90:93]
	v_mov_b32_dpp v129, v128 quad_perm:[1,2,3,0] row_mask:0xf bank_mask:0xf bound_ctrl:1
	v_mov_b32_dpp v130, v128 quad_perm:[2,3,0,1] row_mask:0xf bank_mask:0xf bound_ctrl:1
	v_mfma_f32_16x16x32_f16 v[140:143], v[18:21], v[124:127], v[90:93]
	v_mov_b32_dpp v131, v128 quad_perm:[3,0,1,2] row_mask:0xf bank_mask:0xf bound_ctrl:1
	s_nop 0
	v_mfma_f32_16x16x32_f16 v[144:147], v[26:29], v[124:127], v[90:93]
	v_mfma_f32_16x16x32_f16 v[132:135], v[6:9], v[128:131], v[132:135]
	v_fma_f32 v154, v106, v150, v108
	v_fma_f32 v155, v107, v151, v109
	ds_write_b32 v164, v124 offset:2112
	v_mfma_f32_16x16x32_f16 v[136:139], v[14:17], v[128:131], v[136:139]
	v_fma_f32 v152, v102, v148, v104
	v_fma_f32 v153, v103, v149, v105
	ds_write_b32 v164, v128 offset:2116
	v_mfma_f32_16x16x32_f16 v[140:143], v[22:25], v[128:131], v[140:143]
	global_load_dwordx4 v[90:93], v[0:1], off offset:-768
	s_nop 1
	v_mfma_f32_16x16x32_f16 v[144:147], v[30:33], v[128:131], v[144:147]
	v_cndmask_b32_e64 v160, v136, v132, s[0:1]
	v_cndmask_b32_e64 v161, v137, v133, s[0:1]
	v_cndmask_b32_e64 v162, v138, v134, s[0:1]
	v_cndmask_b32_e64 v163, v139, v135, s[0:1]
	v_cndmask_b32_e64 v160, v140, v160, s[2:3]
	v_cndmask_b32_e64 v161, v141, v161, s[2:3]
	v_cndmask_b32_e64 v162, v142, v162, s[2:3]
	v_cndmask_b32_e64 v163, v143, v163, s[2:3]
	v_cndmask_b32_e64 v156, v160, v144, s[4:5]
	v_cndmask_b32_e64 v157, v161, v145, s[4:5]
	v_exp_f32_e32 v156, v156
	v_exp_f32_e32 v157, v157
	v_cndmask_b32_e64 v158, v162, v146, s[4:5]
	v_cndmask_b32_e64 v159, v163, v147, s[4:5]
	v_pk_add_f32 v[156:157], v[156:157], 1.0 op_sel_hi:[1,0]
	v_exp_f32_e32 v158, v158
	v_rcp_f32_e32 v156, v156
	v_rcp_f32_e32 v157, v157
	v_exp_f32_e32 v159, v159
	v_pk_fma_f32 v[148:149], v[110:111], v[156:157], v[152:153]
	v_pk_add_f32 v[158:159], v[158:159], 1.0 op_sel_hi:[1,0]
	v_cvt_pk_f16_f32 v124, v148, v149
	v_rcp_f32_e32 v158, v158
	v_rcp_f32_e32 v159, v159
	v_mov_b32_dpp v125, v124 quad_perm:[1,2,3,0] row_mask:0xf bank_mask:0xf bound_ctrl:1
	v_mov_b32_dpp v126, v124 quad_perm:[2,3,0,1] row_mask:0xf bank_mask:0xf bound_ctrl:1
	v_mov_b32_dpp v127, v124 quad_perm:[3,0,1,2] row_mask:0xf bank_mask:0xf bound_ctrl:1
	v_pk_fma_f32 v[150:151], v[112:113], v[158:159], v[154:155]
	s_waitcnt vmcnt(15)
	v_mfma_f32_16x16x32_f16 v[132:135], v[2:5], v[124:127], v[82:85]
	v_cvt_pk_f16_f32 v128, v150, v151
	s_nop 0
	v_mfma_f32_16x16x32_f16 v[136:139], v[10:13], v[124:127], v[82:85]
	v_mov_b32_dpp v129, v128 quad_perm:[1,2,3,0] row_mask:0xf bank_mask:0xf bound_ctrl:1
	v_mov_b32_dpp v130, v128 quad_perm:[2,3,0,1] row_mask:0xf bank_mask:0xf bound_ctrl:1
	v_mfma_f32_16x16x32_f16 v[140:143], v[18:21], v[124:127], v[82:85]
	v_mov_b32_dpp v131, v128 quad_perm:[3,0,1,2] row_mask:0xf bank_mask:0xf bound_ctrl:1
	s_nop 0
	v_mfma_f32_16x16x32_f16 v[144:147], v[26:29], v[124:127], v[82:85]
	v_mfma_f32_16x16x32_f16 v[132:135], v[6:9], v[128:131], v[132:135]
	v_fma_f32 v154, v106, v150, v108
	v_fma_f32 v155, v107, v151, v109
	ds_write_b32 v164, v124 offset:2640
	v_mfma_f32_16x16x32_f16 v[136:139], v[14:17], v[128:131], v[136:139]
	v_fma_f32 v152, v102, v148, v104
	v_fma_f32 v153, v103, v149, v105
	ds_write_b32 v164, v128 offset:2644
	v_mfma_f32_16x16x32_f16 v[140:143], v[22:25], v[128:131], v[140:143]
	global_load_dwordx4 v[82:85], v[0:1], off offset:-512
	s_nop 1
	v_mfma_f32_16x16x32_f16 v[144:147], v[30:33], v[128:131], v[144:147]
	v_cndmask_b32_e64 v160, v136, v132, s[0:1]
	v_cndmask_b32_e64 v161, v137, v133, s[0:1]
	v_cndmask_b32_e64 v162, v138, v134, s[0:1]
	v_cndmask_b32_e64 v163, v139, v135, s[0:1]
	v_cndmask_b32_e64 v160, v140, v160, s[2:3]
	v_cndmask_b32_e64 v161, v141, v161, s[2:3]
	v_cndmask_b32_e64 v162, v142, v162, s[2:3]
	v_cndmask_b32_e64 v163, v143, v163, s[2:3]
	v_cndmask_b32_e64 v156, v160, v144, s[4:5]
	v_cndmask_b32_e64 v157, v161, v145, s[4:5]
	v_exp_f32_e32 v156, v156
	v_exp_f32_e32 v157, v157
	v_cndmask_b32_e64 v158, v162, v146, s[4:5]
	v_cndmask_b32_e64 v159, v163, v147, s[4:5]
	v_pk_add_f32 v[156:157], v[156:157], 1.0 op_sel_hi:[1,0]
	v_exp_f32_e32 v158, v158
	v_rcp_f32_e32 v156, v156
	v_rcp_f32_e32 v157, v157
	v_exp_f32_e32 v159, v159
	v_pk_fma_f32 v[148:149], v[110:111], v[156:157], v[152:153]
	v_pk_add_f32 v[158:159], v[158:159], 1.0 op_sel_hi:[1,0]
	v_cvt_pk_f16_f32 v124, v148, v149
	v_rcp_f32_e32 v158, v158
	v_rcp_f32_e32 v159, v159
	v_mov_b32_dpp v125, v124 quad_perm:[1,2,3,0] row_mask:0xf bank_mask:0xf bound_ctrl:1
	v_mov_b32_dpp v126, v124 quad_perm:[2,3,0,1] row_mask:0xf bank_mask:0xf bound_ctrl:1
	v_mov_b32_dpp v127, v124 quad_perm:[3,0,1,2] row_mask:0xf bank_mask:0xf bound_ctrl:1
	v_pk_fma_f32 v[150:151], v[112:113], v[158:159], v[154:155]
	s_waitcnt vmcnt(15)
	v_mfma_f32_16x16x32_f16 v[132:135], v[2:5], v[124:127], v[74:77]
	v_cvt_pk_f16_f32 v128, v150, v151
	s_nop 0
	v_mfma_f32_16x16x32_f16 v[136:139], v[10:13], v[124:127], v[74:77]
	v_mov_b32_dpp v129, v128 quad_perm:[1,2,3,0] row_mask:0xf bank_mask:0xf bound_ctrl:1
	v_mov_b32_dpp v130, v128 quad_perm:[2,3,0,1] row_mask:0xf bank_mask:0xf bound_ctrl:1
	v_mfma_f32_16x16x32_f16 v[140:143], v[18:21], v[124:127], v[74:77]
	v_mov_b32_dpp v131, v128 quad_perm:[3,0,1,2] row_mask:0xf bank_mask:0xf bound_ctrl:1
	s_nop 0
	v_mfma_f32_16x16x32_f16 v[144:147], v[26:29], v[124:127], v[74:77]
	v_mfma_f32_16x16x32_f16 v[132:135], v[6:9], v[128:131], v[132:135]
	v_fma_f32 v154, v106, v150, v108
	v_fma_f32 v155, v107, v151, v109
	ds_write_b32 v164, v124 offset:3168
	v_mfma_f32_16x16x32_f16 v[136:139], v[14:17], v[128:131], v[136:139]
	v_fma_f32 v152, v102, v148, v104
	v_fma_f32 v153, v103, v149, v105
	ds_write_b32 v164, v128 offset:3172
	v_mfma_f32_16x16x32_f16 v[140:143], v[22:25], v[128:131], v[140:143]
	global_load_dwordx4 v[74:77], v[0:1], off offset:-256
	s_nop 1
	v_mfma_f32_16x16x32_f16 v[144:147], v[30:33], v[128:131], v[144:147]
	v_cndmask_b32_e64 v160, v136, v132, s[0:1]
	v_cndmask_b32_e64 v161, v137, v133, s[0:1]
	v_cndmask_b32_e64 v162, v138, v134, s[0:1]
	v_cndmask_b32_e64 v163, v139, v135, s[0:1]
	v_cndmask_b32_e64 v160, v140, v160, s[2:3]
	v_cndmask_b32_e64 v161, v141, v161, s[2:3]
	v_cndmask_b32_e64 v162, v142, v162, s[2:3]
	v_cndmask_b32_e64 v163, v143, v163, s[2:3]
	v_cndmask_b32_e64 v156, v160, v144, s[4:5]
	v_cndmask_b32_e64 v157, v161, v145, s[4:5]
	v_exp_f32_e32 v156, v156
	v_exp_f32_e32 v157, v157
	v_cndmask_b32_e64 v158, v162, v146, s[4:5]
	v_cndmask_b32_e64 v159, v163, v147, s[4:5]
	v_pk_add_f32 v[156:157], v[156:157], 1.0 op_sel_hi:[1,0]
	v_exp_f32_e32 v158, v158
	v_rcp_f32_e32 v156, v156
	v_rcp_f32_e32 v157, v157
	v_exp_f32_e32 v159, v159
	v_pk_fma_f32 v[148:149], v[110:111], v[156:157], v[152:153]
	v_pk_add_f32 v[158:159], v[158:159], 1.0 op_sel_hi:[1,0]
	v_cvt_pk_f16_f32 v124, v148, v149
	v_rcp_f32_e32 v158, v158
	v_rcp_f32_e32 v159, v159
	v_mov_b32_dpp v125, v124 quad_perm:[1,2,3,0] row_mask:0xf bank_mask:0xf bound_ctrl:1
	v_mov_b32_dpp v126, v124 quad_perm:[2,3,0,1] row_mask:0xf bank_mask:0xf bound_ctrl:1
	v_mov_b32_dpp v127, v124 quad_perm:[3,0,1,2] row_mask:0xf bank_mask:0xf bound_ctrl:1
	v_pk_fma_f32 v[150:151], v[112:113], v[158:159], v[154:155]
	s_waitcnt vmcnt(15)
	v_mfma_f32_16x16x32_f16 v[132:135], v[2:5], v[124:127], v[66:69]
	v_cvt_pk_f16_f32 v128, v150, v151
	s_nop 0
	v_mfma_f32_16x16x32_f16 v[136:139], v[10:13], v[124:127], v[66:69]
	v_mov_b32_dpp v129, v128 quad_perm:[1,2,3,0] row_mask:0xf bank_mask:0xf bound_ctrl:1
	v_mov_b32_dpp v130, v128 quad_perm:[2,3,0,1] row_mask:0xf bank_mask:0xf bound_ctrl:1
	v_mfma_f32_16x16x32_f16 v[140:143], v[18:21], v[124:127], v[66:69]
	v_mov_b32_dpp v131, v128 quad_perm:[3,0,1,2] row_mask:0xf bank_mask:0xf bound_ctrl:1
	s_nop 0
	v_mfma_f32_16x16x32_f16 v[144:147], v[26:29], v[124:127], v[66:69]
	v_mfma_f32_16x16x32_f16 v[132:135], v[6:9], v[128:131], v[132:135]
	v_fma_f32 v154, v106, v150, v108
	v_fma_f32 v155, v107, v151, v109
	ds_write_b32 v164, v124 offset:3696
	v_mfma_f32_16x16x32_f16 v[136:139], v[14:17], v[128:131], v[136:139]
	v_fma_f32 v152, v102, v148, v104
	v_fma_f32 v153, v103, v149, v105
	ds_write_b32 v164, v128 offset:3700
	v_mfma_f32_16x16x32_f16 v[140:143], v[22:25], v[128:131], v[140:143]
	global_load_dwordx4 v[66:69], v[0:1], off offset:0
	s_nop 1
	v_mfma_f32_16x16x32_f16 v[144:147], v[30:33], v[128:131], v[144:147]
	v_cndmask_b32_e64 v160, v136, v132, s[0:1]
	v_cndmask_b32_e64 v161, v137, v133, s[0:1]
	v_cndmask_b32_e64 v162, v138, v134, s[0:1]
	v_cndmask_b32_e64 v163, v139, v135, s[0:1]
	v_cndmask_b32_e64 v160, v140, v160, s[2:3]
	v_cndmask_b32_e64 v161, v141, v161, s[2:3]
	v_cndmask_b32_e64 v162, v142, v162, s[2:3]
	v_cndmask_b32_e64 v163, v143, v163, s[2:3]
	v_cndmask_b32_e64 v156, v160, v144, s[4:5]
	v_cndmask_b32_e64 v157, v161, v145, s[4:5]
	v_exp_f32_e32 v156, v156
	v_exp_f32_e32 v157, v157
	v_cndmask_b32_e64 v158, v162, v146, s[4:5]
	v_cndmask_b32_e64 v159, v163, v147, s[4:5]
	v_pk_add_f32 v[156:157], v[156:157], 1.0 op_sel_hi:[1,0]
	v_exp_f32_e32 v158, v158
	v_rcp_f32_e32 v156, v156
	v_rcp_f32_e32 v157, v157
	v_exp_f32_e32 v159, v159
	v_pk_fma_f32 v[148:149], v[110:111], v[156:157], v[152:153]
	v_pk_add_f32 v[158:159], v[158:159], 1.0 op_sel_hi:[1,0]
	v_cvt_pk_f16_f32 v124, v148, v149
	v_rcp_f32_e32 v158, v158
	v_rcp_f32_e32 v159, v159
	v_mov_b32_dpp v125, v124 quad_perm:[1,2,3,0] row_mask:0xf bank_mask:0xf bound_ctrl:1
	v_mov_b32_dpp v126, v124 quad_perm:[2,3,0,1] row_mask:0xf bank_mask:0xf bound_ctrl:1
	v_mov_b32_dpp v127, v124 quad_perm:[3,0,1,2] row_mask:0xf bank_mask:0xf bound_ctrl:1
	v_pk_fma_f32 v[150:151], v[112:113], v[158:159], v[154:155]
	s_waitcnt vmcnt(15)
	v_mfma_f32_16x16x32_f16 v[132:135], v[2:5], v[124:127], v[58:61]
	v_cvt_pk_f16_f32 v128, v150, v151
	s_nop 0
	v_mfma_f32_16x16x32_f16 v[136:139], v[10:13], v[124:127], v[58:61]
	v_mov_b32_dpp v129, v128 quad_perm:[1,2,3,0] row_mask:0xf bank_mask:0xf bound_ctrl:1
	v_mov_b32_dpp v130, v128 quad_perm:[2,3,0,1] row_mask:0xf bank_mask:0xf bound_ctrl:1
	v_mfma_f32_16x16x32_f16 v[140:143], v[18:21], v[124:127], v[58:61]
	v_mov_b32_dpp v131, v128 quad_perm:[3,0,1,2] row_mask:0xf bank_mask:0xf bound_ctrl:1
	s_nop 0
	v_mfma_f32_16x16x32_f16 v[144:147], v[26:29], v[124:127], v[58:61]
	v_mfma_f32_16x16x32_f16 v[132:135], v[6:9], v[128:131], v[132:135]
	v_fma_f32 v154, v106, v150, v108
	v_fma_f32 v155, v107, v151, v109
	ds_write_b32 v164, v124 offset:4224
	v_mfma_f32_16x16x32_f16 v[136:139], v[14:17], v[128:131], v[136:139]
	v_fma_f32 v152, v102, v148, v104
	v_fma_f32 v153, v103, v149, v105
	ds_write_b32 v164, v128 offset:4228
	v_mfma_f32_16x16x32_f16 v[140:143], v[22:25], v[128:131], v[140:143]
	global_load_dwordx4 v[58:61], v[0:1], off offset:256
	s_nop 1
	v_mfma_f32_16x16x32_f16 v[144:147], v[30:33], v[128:131], v[144:147]
	v_cndmask_b32_e64 v160, v136, v132, s[0:1]
	v_cndmask_b32_e64 v161, v137, v133, s[0:1]
	v_cndmask_b32_e64 v162, v138, v134, s[0:1]
	v_cndmask_b32_e64 v163, v139, v135, s[0:1]
	v_cndmask_b32_e64 v160, v140, v160, s[2:3]
	v_cndmask_b32_e64 v161, v141, v161, s[2:3]
	v_cndmask_b32_e64 v162, v142, v162, s[2:3]
	v_cndmask_b32_e64 v163, v143, v163, s[2:3]
	v_cndmask_b32_e64 v156, v160, v144, s[4:5]
	v_cndmask_b32_e64 v157, v161, v145, s[4:5]
	v_exp_f32_e32 v156, v156
	v_exp_f32_e32 v157, v157
	v_cndmask_b32_e64 v158, v162, v146, s[4:5]
	v_cndmask_b32_e64 v159, v163, v147, s[4:5]
	v_pk_add_f32 v[156:157], v[156:157], 1.0 op_sel_hi:[1,0]
	v_exp_f32_e32 v158, v158
	v_rcp_f32_e32 v156, v156
	v_rcp_f32_e32 v157, v157
	v_exp_f32_e32 v159, v159
	v_pk_fma_f32 v[148:149], v[110:111], v[156:157], v[152:153]
	v_pk_add_f32 v[158:159], v[158:159], 1.0 op_sel_hi:[1,0]
	v_cvt_pk_f16_f32 v124, v148, v149
	v_rcp_f32_e32 v158, v158
	v_rcp_f32_e32 v159, v159
	v_mov_b32_dpp v125, v124 quad_perm:[1,2,3,0] row_mask:0xf bank_mask:0xf bound_ctrl:1
	v_mov_b32_dpp v126, v124 quad_perm:[2,3,0,1] row_mask:0xf bank_mask:0xf bound_ctrl:1
	v_mov_b32_dpp v127, v124 quad_perm:[3,0,1,2] row_mask:0xf bank_mask:0xf bound_ctrl:1
	v_pk_fma_f32 v[150:151], v[112:113], v[158:159], v[154:155]
	s_waitcnt vmcnt(15)
	v_mfma_f32_16x16x32_f16 v[132:135], v[2:5], v[124:127], v[54:57]
	v_cvt_pk_f16_f32 v128, v150, v151
	s_nop 0
	v_mfma_f32_16x16x32_f16 v[136:139], v[10:13], v[124:127], v[54:57]
	v_mov_b32_dpp v129, v128 quad_perm:[1,2,3,0] row_mask:0xf bank_mask:0xf bound_ctrl:1
	v_mov_b32_dpp v130, v128 quad_perm:[2,3,0,1] row_mask:0xf bank_mask:0xf bound_ctrl:1
	v_mfma_f32_16x16x32_f16 v[140:143], v[18:21], v[124:127], v[54:57]
	v_mov_b32_dpp v131, v128 quad_perm:[3,0,1,2] row_mask:0xf bank_mask:0xf bound_ctrl:1
	s_nop 0
	v_mfma_f32_16x16x32_f16 v[144:147], v[26:29], v[124:127], v[54:57]
	v_mfma_f32_16x16x32_f16 v[132:135], v[6:9], v[128:131], v[132:135]
	v_fma_f32 v154, v106, v150, v108
	v_fma_f32 v155, v107, v151, v109
	ds_write_b32 v164, v124 offset:4752
	v_mfma_f32_16x16x32_f16 v[136:139], v[14:17], v[128:131], v[136:139]
	v_fma_f32 v152, v102, v148, v104
	v_fma_f32 v153, v103, v149, v105
	ds_write_b32 v164, v128 offset:4756
	v_mfma_f32_16x16x32_f16 v[140:143], v[22:25], v[128:131], v[140:143]
	global_load_dwordx4 v[54:57], v[0:1], off offset:512
	s_nop 1
	v_mfma_f32_16x16x32_f16 v[144:147], v[30:33], v[128:131], v[144:147]
	v_cndmask_b32_e64 v160, v136, v132, s[0:1]
	v_cndmask_b32_e64 v161, v137, v133, s[0:1]
	v_cndmask_b32_e64 v162, v138, v134, s[0:1]
	v_cndmask_b32_e64 v163, v139, v135, s[0:1]
	v_cndmask_b32_e64 v160, v140, v160, s[2:3]
	v_cndmask_b32_e64 v161, v141, v161, s[2:3]
	v_cndmask_b32_e64 v162, v142, v162, s[2:3]
	v_cndmask_b32_e64 v163, v143, v163, s[2:3]
	v_cndmask_b32_e64 v156, v160, v144, s[4:5]
	v_cndmask_b32_e64 v157, v161, v145, s[4:5]
	v_exp_f32_e32 v156, v156
	v_exp_f32_e32 v157, v157
	v_cndmask_b32_e64 v158, v162, v146, s[4:5]
	v_cndmask_b32_e64 v159, v163, v147, s[4:5]
	v_pk_add_f32 v[156:157], v[156:157], 1.0 op_sel_hi:[1,0]
	v_exp_f32_e32 v158, v158
	v_rcp_f32_e32 v156, v156
	v_rcp_f32_e32 v157, v157
	v_exp_f32_e32 v159, v159
	v_pk_fma_f32 v[148:149], v[110:111], v[156:157], v[152:153]
	v_pk_add_f32 v[158:159], v[158:159], 1.0 op_sel_hi:[1,0]
	v_cvt_pk_f16_f32 v124, v148, v149
	v_rcp_f32_e32 v158, v158
	v_rcp_f32_e32 v159, v159
	v_mov_b32_dpp v125, v124 quad_perm:[1,2,3,0] row_mask:0xf bank_mask:0xf bound_ctrl:1
	v_mov_b32_dpp v126, v124 quad_perm:[2,3,0,1] row_mask:0xf bank_mask:0xf bound_ctrl:1
	v_mov_b32_dpp v127, v124 quad_perm:[3,0,1,2] row_mask:0xf bank_mask:0xf bound_ctrl:1
	v_pk_fma_f32 v[150:151], v[112:113], v[158:159], v[154:155]
	s_waitcnt vmcnt(15)
	v_mfma_f32_16x16x32_f16 v[132:135], v[2:5], v[124:127], v[50:53]
	v_cvt_pk_f16_f32 v128, v150, v151
	s_nop 0
	v_mfma_f32_16x16x32_f16 v[136:139], v[10:13], v[124:127], v[50:53]
	v_mov_b32_dpp v129, v128 quad_perm:[1,2,3,0] row_mask:0xf bank_mask:0xf bound_ctrl:1
	v_mov_b32_dpp v130, v128 quad_perm:[2,3,0,1] row_mask:0xf bank_mask:0xf bound_ctrl:1
	v_mfma_f32_16x16x32_f16 v[140:143], v[18:21], v[124:127], v[50:53]
	v_mov_b32_dpp v131, v128 quad_perm:[3,0,1,2] row_mask:0xf bank_mask:0xf bound_ctrl:1
	s_nop 0
	v_mfma_f32_16x16x32_f16 v[144:147], v[26:29], v[124:127], v[50:53]
	v_mfma_f32_16x16x32_f16 v[132:135], v[6:9], v[128:131], v[132:135]
	v_fma_f32 v154, v106, v150, v108
	v_fma_f32 v155, v107, v151, v109
	ds_write_b32 v164, v124 offset:5280
	v_mfma_f32_16x16x32_f16 v[136:139], v[14:17], v[128:131], v[136:139]
	v_fma_f32 v152, v102, v148, v104
	v_fma_f32 v153, v103, v149, v105
	ds_write_b32 v164, v128 offset:5284
	v_mfma_f32_16x16x32_f16 v[140:143], v[22:25], v[128:131], v[140:143]
	global_load_dwordx4 v[50:53], v[0:1], off offset:768
	s_nop 1
	v_mfma_f32_16x16x32_f16 v[144:147], v[30:33], v[128:131], v[144:147]
	v_cndmask_b32_e64 v160, v136, v132, s[0:1]
	v_cndmask_b32_e64 v161, v137, v133, s[0:1]
	v_cndmask_b32_e64 v162, v138, v134, s[0:1]
	v_cndmask_b32_e64 v163, v139, v135, s[0:1]
	v_cndmask_b32_e64 v160, v140, v160, s[2:3]
	v_cndmask_b32_e64 v161, v141, v161, s[2:3]
	v_cndmask_b32_e64 v162, v142, v162, s[2:3]
	v_cndmask_b32_e64 v163, v143, v163, s[2:3]
	v_cndmask_b32_e64 v156, v160, v144, s[4:5]
	v_cndmask_b32_e64 v157, v161, v145, s[4:5]
	v_exp_f32_e32 v156, v156
	v_exp_f32_e32 v157, v157
	v_cndmask_b32_e64 v158, v162, v146, s[4:5]
	v_cndmask_b32_e64 v159, v163, v147, s[4:5]
	v_pk_add_f32 v[156:157], v[156:157], 1.0 op_sel_hi:[1,0]
	v_exp_f32_e32 v158, v158
	v_rcp_f32_e32 v156, v156
	v_rcp_f32_e32 v157, v157
	v_exp_f32_e32 v159, v159
	v_pk_fma_f32 v[148:149], v[110:111], v[156:157], v[152:153]
	v_pk_add_f32 v[158:159], v[158:159], 1.0 op_sel_hi:[1,0]
	v_cvt_pk_f16_f32 v124, v148, v149
	v_rcp_f32_e32 v158, v158
	v_rcp_f32_e32 v159, v159
	v_mov_b32_dpp v125, v124 quad_perm:[1,2,3,0] row_mask:0xf bank_mask:0xf bound_ctrl:1
	v_mov_b32_dpp v126, v124 quad_perm:[2,3,0,1] row_mask:0xf bank_mask:0xf bound_ctrl:1
	v_mov_b32_dpp v127, v124 quad_perm:[3,0,1,2] row_mask:0xf bank_mask:0xf bound_ctrl:1
	v_pk_fma_f32 v[150:151], v[112:113], v[158:159], v[154:155]
	s_waitcnt vmcnt(15)
	v_mfma_f32_16x16x32_f16 v[132:135], v[2:5], v[124:127], v[46:49]
	v_cvt_pk_f16_f32 v128, v150, v151
	s_nop 0
	v_mfma_f32_16x16x32_f16 v[136:139], v[10:13], v[124:127], v[46:49]
	v_mov_b32_dpp v129, v128 quad_perm:[1,2,3,0] row_mask:0xf bank_mask:0xf bound_ctrl:1
	v_mov_b32_dpp v130, v128 quad_perm:[2,3,0,1] row_mask:0xf bank_mask:0xf bound_ctrl:1
	v_mfma_f32_16x16x32_f16 v[140:143], v[18:21], v[124:127], v[46:49]
	v_mov_b32_dpp v131, v128 quad_perm:[3,0,1,2] row_mask:0xf bank_mask:0xf bound_ctrl:1
	s_nop 0
	v_mfma_f32_16x16x32_f16 v[144:147], v[26:29], v[124:127], v[46:49]
	v_mfma_f32_16x16x32_f16 v[132:135], v[6:9], v[128:131], v[132:135]
	v_fma_f32 v154, v106, v150, v108
	v_fma_f32 v155, v107, v151, v109
	ds_write_b32 v164, v124 offset:5808
	v_mfma_f32_16x16x32_f16 v[136:139], v[14:17], v[128:131], v[136:139]
	v_fma_f32 v152, v102, v148, v104
	v_fma_f32 v153, v103, v149, v105
	ds_write_b32 v164, v128 offset:5812
	v_mfma_f32_16x16x32_f16 v[140:143], v[22:25], v[128:131], v[140:143]
	global_load_dwordx4 v[46:49], v[0:1], off offset:1024
	s_nop 1
	v_mfma_f32_16x16x32_f16 v[144:147], v[30:33], v[128:131], v[144:147]
	v_cndmask_b32_e64 v160, v136, v132, s[0:1]
	v_cndmask_b32_e64 v161, v137, v133, s[0:1]
	v_cndmask_b32_e64 v162, v138, v134, s[0:1]
	v_cndmask_b32_e64 v163, v139, v135, s[0:1]
	v_cndmask_b32_e64 v160, v140, v160, s[2:3]
	v_cndmask_b32_e64 v161, v141, v161, s[2:3]
	v_cndmask_b32_e64 v162, v142, v162, s[2:3]
	v_cndmask_b32_e64 v163, v143, v163, s[2:3]
	v_cndmask_b32_e64 v156, v160, v144, s[4:5]
	v_cndmask_b32_e64 v157, v161, v145, s[4:5]
	v_exp_f32_e32 v156, v156
	v_exp_f32_e32 v157, v157
	v_cndmask_b32_e64 v158, v162, v146, s[4:5]
	v_cndmask_b32_e64 v159, v163, v147, s[4:5]
	v_pk_add_f32 v[156:157], v[156:157], 1.0 op_sel_hi:[1,0]
	v_exp_f32_e32 v158, v158
	v_rcp_f32_e32 v156, v156
	v_rcp_f32_e32 v157, v157
	v_exp_f32_e32 v159, v159
	v_pk_fma_f32 v[148:149], v[110:111], v[156:157], v[152:153]
	v_pk_add_f32 v[158:159], v[158:159], 1.0 op_sel_hi:[1,0]
	v_cvt_pk_f16_f32 v124, v148, v149
	v_rcp_f32_e32 v158, v158
	v_rcp_f32_e32 v159, v159
	v_mov_b32_dpp v125, v124 quad_perm:[1,2,3,0] row_mask:0xf bank_mask:0xf bound_ctrl:1
	v_mov_b32_dpp v126, v124 quad_perm:[2,3,0,1] row_mask:0xf bank_mask:0xf bound_ctrl:1
	v_mov_b32_dpp v127, v124 quad_perm:[3,0,1,2] row_mask:0xf bank_mask:0xf bound_ctrl:1
	v_pk_fma_f32 v[150:151], v[112:113], v[158:159], v[154:155]
	s_waitcnt vmcnt(15)
	v_mfma_f32_16x16x32_f16 v[132:135], v[2:5], v[124:127], v[42:45]
	v_cvt_pk_f16_f32 v128, v150, v151
	s_nop 0
	v_mfma_f32_16x16x32_f16 v[136:139], v[10:13], v[124:127], v[42:45]
	v_mov_b32_dpp v129, v128 quad_perm:[1,2,3,0] row_mask:0xf bank_mask:0xf bound_ctrl:1
	v_mov_b32_dpp v130, v128 quad_perm:[2,3,0,1] row_mask:0xf bank_mask:0xf bound_ctrl:1
	v_mfma_f32_16x16x32_f16 v[140:143], v[18:21], v[124:127], v[42:45]
	v_mov_b32_dpp v131, v128 quad_perm:[3,0,1,2] row_mask:0xf bank_mask:0xf bound_ctrl:1
	s_nop 0
	v_mfma_f32_16x16x32_f16 v[144:147], v[26:29], v[124:127], v[42:45]
	v_mfma_f32_16x16x32_f16 v[132:135], v[6:9], v[128:131], v[132:135]
	v_fma_f32 v154, v106, v150, v108
	v_fma_f32 v155, v107, v151, v109
	ds_write_b32 v164, v124 offset:6336
	v_mfma_f32_16x16x32_f16 v[136:139], v[14:17], v[128:131], v[136:139]
	v_fma_f32 v152, v102, v148, v104
	v_fma_f32 v153, v103, v149, v105
	ds_write_b32 v164, v128 offset:6340
	v_mfma_f32_16x16x32_f16 v[140:143], v[22:25], v[128:131], v[140:143]
	global_load_dwordx4 v[42:45], v[0:1], off offset:1280
	s_nop 1
	v_mfma_f32_16x16x32_f16 v[144:147], v[30:33], v[128:131], v[144:147]
	v_cndmask_b32_e64 v160, v136, v132, s[0:1]
	v_cndmask_b32_e64 v161, v137, v133, s[0:1]
	v_cndmask_b32_e64 v162, v138, v134, s[0:1]
	v_cndmask_b32_e64 v163, v139, v135, s[0:1]
	v_cndmask_b32_e64 v160, v140, v160, s[2:3]
	v_cndmask_b32_e64 v161, v141, v161, s[2:3]
	v_cndmask_b32_e64 v162, v142, v162, s[2:3]
	v_cndmask_b32_e64 v163, v143, v163, s[2:3]
	v_cndmask_b32_e64 v156, v160, v144, s[4:5]
	v_cndmask_b32_e64 v157, v161, v145, s[4:5]
	v_exp_f32_e32 v156, v156
	v_exp_f32_e32 v157, v157
	v_cndmask_b32_e64 v158, v162, v146, s[4:5]
	v_cndmask_b32_e64 v159, v163, v147, s[4:5]
	v_pk_add_f32 v[156:157], v[156:157], 1.0 op_sel_hi:[1,0]
	v_exp_f32_e32 v158, v158
	v_rcp_f32_e32 v156, v156
	v_rcp_f32_e32 v157, v157
	v_exp_f32_e32 v159, v159
	v_pk_fma_f32 v[148:149], v[110:111], v[156:157], v[152:153]
	v_pk_add_f32 v[158:159], v[158:159], 1.0 op_sel_hi:[1,0]
	v_cvt_pk_f16_f32 v124, v148, v149
	v_rcp_f32_e32 v158, v158
	v_rcp_f32_e32 v159, v159
	v_mov_b32_dpp v125, v124 quad_perm:[1,2,3,0] row_mask:0xf bank_mask:0xf bound_ctrl:1
	v_mov_b32_dpp v126, v124 quad_perm:[2,3,0,1] row_mask:0xf bank_mask:0xf bound_ctrl:1
	v_mov_b32_dpp v127, v124 quad_perm:[3,0,1,2] row_mask:0xf bank_mask:0xf bound_ctrl:1
	v_pk_fma_f32 v[150:151], v[112:113], v[158:159], v[154:155]
	s_waitcnt vmcnt(15)
	v_mfma_f32_16x16x32_f16 v[132:135], v[2:5], v[124:127], v[38:41]
	v_cvt_pk_f16_f32 v128, v150, v151
	s_nop 0
	v_mfma_f32_16x16x32_f16 v[136:139], v[10:13], v[124:127], v[38:41]
	v_mov_b32_dpp v129, v128 quad_perm:[1,2,3,0] row_mask:0xf bank_mask:0xf bound_ctrl:1
	v_mov_b32_dpp v130, v128 quad_perm:[2,3,0,1] row_mask:0xf bank_mask:0xf bound_ctrl:1
	v_mfma_f32_16x16x32_f16 v[140:143], v[18:21], v[124:127], v[38:41]
	v_mov_b32_dpp v131, v128 quad_perm:[3,0,1,2] row_mask:0xf bank_mask:0xf bound_ctrl:1
	s_nop 0
	v_mfma_f32_16x16x32_f16 v[144:147], v[26:29], v[124:127], v[38:41]
	v_mfma_f32_16x16x32_f16 v[132:135], v[6:9], v[128:131], v[132:135]
	v_fma_f32 v154, v106, v150, v108
	v_fma_f32 v155, v107, v151, v109
	ds_write_b32 v164, v124 offset:6864
	v_mfma_f32_16x16x32_f16 v[136:139], v[14:17], v[128:131], v[136:139]
	v_fma_f32 v152, v102, v148, v104
	v_fma_f32 v153, v103, v149, v105
	ds_write_b32 v164, v128 offset:6868
	v_mfma_f32_16x16x32_f16 v[140:143], v[22:25], v[128:131], v[140:143]
	global_load_dwordx4 v[38:41], v[0:1], off offset:1536
	s_nop 1
	v_mfma_f32_16x16x32_f16 v[144:147], v[30:33], v[128:131], v[144:147]
	v_cndmask_b32_e64 v160, v136, v132, s[0:1]
	v_cndmask_b32_e64 v161, v137, v133, s[0:1]
	v_cndmask_b32_e64 v162, v138, v134, s[0:1]
	v_cndmask_b32_e64 v163, v139, v135, s[0:1]
	v_cndmask_b32_e64 v160, v140, v160, s[2:3]
	v_cndmask_b32_e64 v161, v141, v161, s[2:3]
	v_cndmask_b32_e64 v162, v142, v162, s[2:3]
	v_cndmask_b32_e64 v163, v143, v163, s[2:3]
	v_cndmask_b32_e64 v156, v160, v144, s[4:5]
	v_cndmask_b32_e64 v157, v161, v145, s[4:5]
	v_exp_f32_e32 v156, v156
	v_exp_f32_e32 v157, v157
	v_cndmask_b32_e64 v158, v162, v146, s[4:5]
	v_cndmask_b32_e64 v159, v163, v147, s[4:5]
	v_pk_add_f32 v[156:157], v[156:157], 1.0 op_sel_hi:[1,0]
	v_exp_f32_e32 v158, v158
	v_rcp_f32_e32 v156, v156
	v_rcp_f32_e32 v157, v157
	v_exp_f32_e32 v159, v159
	v_pk_fma_f32 v[148:149], v[110:111], v[156:157], v[152:153]
	v_pk_add_f32 v[158:159], v[158:159], 1.0 op_sel_hi:[1,0]
	v_cvt_pk_f16_f32 v124, v148, v149
	v_rcp_f32_e32 v158, v158
	v_rcp_f32_e32 v159, v159
	v_mov_b32_dpp v125, v124 quad_perm:[1,2,3,0] row_mask:0xf bank_mask:0xf bound_ctrl:1
	v_mov_b32_dpp v126, v124 quad_perm:[2,3,0,1] row_mask:0xf bank_mask:0xf bound_ctrl:1
	v_mov_b32_dpp v127, v124 quad_perm:[3,0,1,2] row_mask:0xf bank_mask:0xf bound_ctrl:1
	v_pk_fma_f32 v[150:151], v[112:113], v[158:159], v[154:155]
	s_waitcnt vmcnt(15)
	v_mfma_f32_16x16x32_f16 v[132:135], v[2:5], v[124:127], v[34:37]
	v_cvt_pk_f16_f32 v128, v150, v151
	s_nop 0
	v_mfma_f32_16x16x32_f16 v[136:139], v[10:13], v[124:127], v[34:37]
	v_mov_b32_dpp v129, v128 quad_perm:[1,2,3,0] row_mask:0xf bank_mask:0xf bound_ctrl:1
	v_mov_b32_dpp v130, v128 quad_perm:[2,3,0,1] row_mask:0xf bank_mask:0xf bound_ctrl:1
	v_mfma_f32_16x16x32_f16 v[140:143], v[18:21], v[124:127], v[34:37]
	v_mov_b32_dpp v131, v128 quad_perm:[3,0,1,2] row_mask:0xf bank_mask:0xf bound_ctrl:1
	s_nop 0
	v_mfma_f32_16x16x32_f16 v[144:147], v[26:29], v[124:127], v[34:37]
	v_mfma_f32_16x16x32_f16 v[132:135], v[6:9], v[128:131], v[132:135]
	v_fma_f32 v154, v106, v150, v108
	v_fma_f32 v155, v107, v151, v109
	ds_write_b32 v164, v124 offset:7392
	v_mfma_f32_16x16x32_f16 v[136:139], v[14:17], v[128:131], v[136:139]
	v_fma_f32 v152, v102, v148, v104
	v_fma_f32 v153, v103, v149, v105
	ds_write_b32 v164, v128 offset:7396
	v_mfma_f32_16x16x32_f16 v[140:143], v[22:25], v[128:131], v[140:143]
	global_load_dwordx4 v[34:37], v[0:1], off offset:1792
	s_nop 1
	v_mfma_f32_16x16x32_f16 v[144:147], v[30:33], v[128:131], v[144:147]
	v_cndmask_b32_e64 v160, v136, v132, s[0:1]
	v_cndmask_b32_e64 v161, v137, v133, s[0:1]
	v_cndmask_b32_e64 v162, v138, v134, s[0:1]
	v_cndmask_b32_e64 v163, v139, v135, s[0:1]
	v_cndmask_b32_e64 v160, v140, v160, s[2:3]
	v_cndmask_b32_e64 v161, v141, v161, s[2:3]
	v_cndmask_b32_e64 v162, v142, v162, s[2:3]
	v_cndmask_b32_e64 v163, v143, v163, s[2:3]
	v_cndmask_b32_e64 v156, v160, v144, s[4:5]
	v_cndmask_b32_e64 v157, v161, v145, s[4:5]
	v_exp_f32_e32 v156, v156
	v_exp_f32_e32 v157, v157
	v_cndmask_b32_e64 v158, v162, v146, s[4:5]
	v_cndmask_b32_e64 v159, v163, v147, s[4:5]
	v_pk_add_f32 v[156:157], v[156:157], 1.0 op_sel_hi:[1,0]
	v_exp_f32_e32 v158, v158
	v_rcp_f32_e32 v156, v156
	v_rcp_f32_e32 v157, v157
	v_exp_f32_e32 v159, v159
	v_pk_fma_f32 v[148:149], v[110:111], v[156:157], v[152:153]
	v_pk_add_f32 v[158:159], v[158:159], 1.0 op_sel_hi:[1,0]
	v_cvt_pk_f16_f32 v124, v148, v149
	v_rcp_f32_e32 v158, v158
	v_rcp_f32_e32 v159, v159
	v_mov_b32_dpp v125, v124 quad_perm:[1,2,3,0] row_mask:0xf bank_mask:0xf bound_ctrl:1
	v_mov_b32_dpp v126, v124 quad_perm:[2,3,0,1] row_mask:0xf bank_mask:0xf bound_ctrl:1
	v_mov_b32_dpp v127, v124 quad_perm:[3,0,1,2] row_mask:0xf bank_mask:0xf bound_ctrl:1
	v_pk_fma_f32 v[150:151], v[112:113], v[158:159], v[154:155]
	s_nop 0
	v_cvt_pk_f16_f32 v128, v150, v151
	ds_write_b32 v164, v124 offset:7920
	v_fma_f32 v152, v102, v148, v104
	v_mov_b32_dpp v129, v128 quad_perm:[1,2,3,0] row_mask:0xf bank_mask:0xf bound_ctrl:1
	v_mov_b32_dpp v130, v128 quad_perm:[2,3,0,1] row_mask:0xf bank_mask:0xf bound_ctrl:1
	v_mov_b32_dpp v131, v128 quad_perm:[3,0,1,2] row_mask:0xf bank_mask:0xf bound_ctrl:1
	ds_write_b32 v164, v128 offset:7924
	v_fma_f32 v153, v103, v149, v105
	v_fma_f32 v154, v106, v150, v108
	v_fma_f32 v155, v107, v151, v109
	s_branch .LBB3_168
